# attention row sums: 10 additive-identity starts (0 + x) folded into the next add; 3 mov+fmac pairs -> v_fmamk_f32 (bit-identical)
# speedup vs baseline: 1.0080x; 1.0080x over previous
; template <int MODE>
; __device__ __forceinline__ void partialSM(f32x16& p0, f32x16& p1, float& m_reg, float& mn, float& alpha) {
;     ...
;     constexpr float C2 = 1.4426950408889634f * SCALE;
;     if (__builtin_expect(__all((pmax - m_reg) * SCALE <= THR), 1)) { mn = m_reg; alpha = 1.f; }
;     else { mn = fmaxf(m_reg, pmax); alpha = __builtin_amdgcn_exp2f((m_reg - mn) * C2); m_reg = mn; }
;     const float mnL = -mn * C2;
; #pragma unroll
;     for (int r = 0; r < 16; ++r) p0[r] = fmaf(p0[r], C2, mnL);
; #pragma unroll
;     for (int r = 0; r < 16; ++r) p1[r] = fmaf(p1[r], C2, mnL);
; #pragma unroll
;     for (int r = 0; r < 16; ++r) p0[r] = __builtin_amdgcn_exp2f(p0[r]);
; template <int KB, bool SK, bool ROPE, bool QHALF>
; __device__ __forceinline__ void qkt(f32x16& p0, f32x16& p1, const char* lds, int r32, int hi, const bf16x8* qr, const char* qrl, bool act) {
;     ...
;     const char* kb[4];
; #pragma unroll
;     for (int dd = 0; dd < 4; ++dd) kb[dd] = lds + OFF_K + KB * SHM_K + KSWZ(r32, (dd * 16 + hi * 8) * 2);
; #pragma unroll
;     for (int d0 = 0; d0 < 8; ++d0) { const char* a = kb[d0 & 3] + (d0 >> 2) * 128;
;         bf16x8 b0 = *reinterpret_cast<const bf16x8*>(a);
;         bf16x8 b1 = *reinterpret_cast<const bf16x8*>(a + 32 * 256);
;         bf16x8 qf;
;         if constexpr (QHALF) { if (d0 >= 4) qf = *reinterpret_cast<const bf16x8*>(qrl + (d0 - 4) * 1024); else qf = qr[d0]; } else qf = qr[d0];
;         p0 = __builtin_amdgcn_mfma_f32_32x32x16_bf16(b0, qf, p0, 0, 0, 0);
;         p1 = __builtin_amdgcn_mfma_f32_32x32x16_bf16(b1, qf, p1, 0, 0, 0); }
.LBB0_524:
	v_cndmask_b32_e64 v178, v5, v228, s[6:7]
	v_mul_f32_e32 v6, 0xbdd53b94, v178
	v_fmamk_f32 v13, v137, 0x3dd53b94, v6
	v_fmamk_f32 v137, v141, 0x3dd53b94, v6
	v_fmamk_f32 v5, v130, 0x3dd53b94, v6
	v_fmamk_f32 v7, v131, 0x3dd53b94, v6
	v_fmamk_f32 v8, v132, 0x3dd53b94, v6
	v_fmamk_f32 v9, v133, 0x3dd53b94, v6
	v_fmamk_f32 v10, v134, 0x3dd53b94, v6
	v_fmamk_f32 v11, v135, 0x3dd53b94, v6
	v_fmamk_f32 v12, v136, 0x3dd53b94, v6
	v_fmamk_f32 v14, v138, 0x3dd53b94, v6
	v_fmamk_f32 v15, v139, 0x3dd53b94, v6
	v_fmamk_f32 v136, v140, 0x3dd53b94, v6
	v_fmamk_f32 v138, v142, 0x3dd53b94, v6
	v_fmamk_f32 v139, v143, 0x3dd53b94, v6
	v_fmamk_f32 v140, v144, 0x3dd53b94, v6
	v_fmamk_f32 v141, v145, 0x3dd53b94, v6
	v_exp_f32_e32 v188, v5
	v_exp_f32_e32 v228, v7
	v_exp_f32_e32 v186, v8
	v_exp_f32_e32 v189, v9
	v_exp_f32_e32 v185, v10
	v_exp_f32_e32 v187, v11
	v_exp_f32_e32 v183, v12
	v_exp_f32_e32 v184, v13
	v_exp_f32_e32 v179, v14
	v_exp_f32_e32 v182, v15
	v_exp_f32_e32 v144, v136
	v_exp_f32_e32 v180, v137
	v_exp_f32_e32 v142, v138
	v_exp_f32_e32 v181, v139
	v_exp_f32_e32 v143, v140
	v_exp_f32_e32 v145, v141
	v_add_f32_e32 v5, v195, v226
	v_fmac_f32_e32 v5, v221, v191
	v_add_f32_e32 v191, v229, v230
	s_addk_i32 s48, 0x80
	s_add_i32 s36, s36, 2
	v_pk_fma_f32 v[128:129], v[128:129], s[22:23], v[6:7] op_sel_hi:[1,0,0]
	v_pk_fma_f32 v[126:127], v[126:127], s[22:23], v[6:7] op_sel_hi:[1,0,0]
	v_pk_fma_f32 v[130:131], v[124:125], s[22:23], v[6:7] op_sel_hi:[1,0,0]
	v_pk_fma_f32 v[132:133], v[122:123], s[22:23], v[6:7] op_sel_hi:[1,0,0]
	v_pk_fma_f32 v[134:135], v[120:121], s[22:23], v[6:7] op_sel_hi:[1,0,0]
	v_pk_fma_f32 v[136:137], v[118:119], s[22:23], v[6:7] op_sel_hi:[1,0,0]
	v_pk_fma_f32 v[138:139], v[116:117], s[22:23], v[6:7] op_sel_hi:[1,0,0]
	v_pk_fma_f32 v[140:141], v[114:115], s[22:23], v[6:7] op_sel_hi:[1,0,0]
	v_fmac_f32_e32 v191, v5, v227
	s_cmp_ge_i32 s36, s71
	v_add_u32_e32 v193, 0xffffff80, v193
	v_mov_b32_e32 v221, v4
	s_waitcnt lgkmcnt(0)
	s_cbranch_scc0 .Lmy_nobar_0
	s_barrier
	s_branch .LBB0_541
.Lmy_nobar_0:
.LBB0_525:
	ds_read_b128 v[4:7], v213 offset:49152
	ds_read_b128 v[8:11], v213 offset:57344
	s_add_i32 s10, 0, 0x12800
	v_exp_f32_e32 v122, v132
	v_exp_f32_e32 v123, v133
	s_waitcnt lgkmcnt(1)
	v_mfma_f32_32x32x16_bf16 v[102:117], v[4:7], v[174:177], 0
	v_exp_f32_e32 v124, v130
	v_exp_f32_e32 v125, v131
	v_exp_f32_e32 v126, v126
	v_exp_f32_e32 v127, v127
	v_exp_f32_e32 v128, v128
	v_exp_f32_e32 v129, v129
	s_add_i32 s6, s48, 0xffffff60
	s_waitcnt lgkmcnt(0)
	v_mfma_f32_32x32x16_bf16 v[86:101], v[8:11], v[174:177], 0
	ds_read_b128 v[4:7], v214 offset:49152
	ds_read_b128 v[8:11], v214 offset:57344
	s_add_i32 s7, s48, 0xffffff9f
	s_waitcnt lgkmcnt(1)
	v_mfma_f32_32x32x16_bf16 v[102:117], v[4:7], v[170:173], v[102:117]
	s_waitcnt lgkmcnt(0)
	v_mfma_f32_32x32x16_bf16 v[86:101], v[8:11], v[170:173], v[86:101]
	ds_read_b128 v[4:7], v215 offset:49152
	ds_read_b128 v[8:11], v215 offset:57344
	s_waitcnt lgkmcnt(1)
	v_mfma_f32_32x32x16_bf16 v[102:117], v[4:7], v[166:169], v[102:117]
	s_waitcnt lgkmcnt(0)
	v_mfma_f32_32x32x16_bf16 v[86:101], v[8:11], v[166:169], v[86:101]
	ds_read_b128 v[4:7], v216 offset:49152
	ds_read_b128 v[8:11], v216 offset:57344
	s_waitcnt lgkmcnt(1)
	v_mfma_f32_32x32x16_bf16 v[102:117], v[4:7], v[162:165], v[102:117]
	s_waitcnt lgkmcnt(0)
	v_mfma_f32_32x32x16_bf16 v[86:101], v[8:11], v[162:165], v[86:101]
	ds_read_b128 v[4:7], v213 offset:49280
	ds_read_b128 v[8:11], v213 offset:57472
	s_waitcnt lgkmcnt(1)
	v_mfma_f32_32x32x16_bf16 v[102:117], v[4:7], v[158:161], v[102:117]
	s_waitcnt lgkmcnt(0)
	v_mfma_f32_32x32x16_bf16 v[86:101], v[8:11], v[158:161], v[86:101]
	ds_read_b128 v[4:7], v214 offset:49280
	ds_read_b128 v[8:11], v214 offset:57472
	s_waitcnt lgkmcnt(1)
	v_mfma_f32_32x32x16_bf16 v[102:117], v[4:7], v[154:157], v[102:117]
	s_waitcnt lgkmcnt(0)
	v_mfma_f32_32x32x16_bf16 v[86:101], v[8:11], v[154:157], v[86:101]
	ds_read_b128 v[4:7], v215 offset:49280
	ds_read_b128 v[8:11], v215 offset:57472
	s_waitcnt lgkmcnt(1)
	v_mfma_f32_32x32x16_bf16 v[102:117], v[4:7], v[150:153], v[102:117]
	s_waitcnt lgkmcnt(0)
	v_mfma_f32_32x32x16_bf16 v[86:101], v[8:11], v[150:153], v[86:101]
	ds_read_b128 v[4:7], v216 offset:49280
	ds_read_b128 v[8:11], v216 offset:57472
	s_waitcnt lgkmcnt(1)
	v_mfma_f32_32x32x16_bf16 v[102:117], v[4:7], v[146:149], v[102:117]
	s_waitcnt lgkmcnt(0)
	v_mfma_f32_32x32x16_bf16 v[86:101], v[8:11], v[146:149], v[86:101]
	v_add_u32_e32 v8, s10, v217
	ds_read_b128 v[4:7], v8
	ds_read_b128 v[8:11], v8 offset:4096
	ds_read_b128 v[12:15], v202
	s_waitcnt lgkmcnt(0)
	v_mfma_f32_32x32x16_bf16 v[102:117], v[4:7], v[12:15], v[102:117]
	v_mfma_f32_32x32x16_bf16 v[86:101], v[8:11], v[12:15], v[86:101]
	v_add_u32_e32 v8, s10, v218
	ds_read_b128 v[4:7], v8
	ds_read_b128 v[8:11], v8 offset:4096
	ds_read_b128 v[12:15], v202 offset:1024
	s_waitcnt lgkmcnt(0)
	v_mfma_f32_32x32x16_bf16 v[102:117], v[4:7], v[12:15], v[102:117]
	v_mfma_f32_32x32x16_bf16 v[86:101], v[8:11], v[12:15], v[86:101]
	v_add_u32_e32 v8, s10, v219
	ds_read_b128 v[4:7], v8
	ds_read_b128 v[8:11], v8 offset:4096
	ds_read_b128 v[12:15], v202 offset:2048
	s_waitcnt lgkmcnt(0)
	v_mfma_f32_32x32x16_bf16 v[102:117], v[4:7], v[12:15], v[102:117]
	v_mfma_f32_32x32x16_bf16 v[86:101], v[8:11], v[12:15], v[86:101]
	v_add_u32_e32 v8, s10, v220
	ds_read_b128 v[4:7], v8
	ds_read_b128 v[8:11], v8 offset:4096
	ds_read_b128 v[12:15], v202 offset:3072
	s_waitcnt lgkmcnt(0)
; __device__ __forceinline__ void finishSM(f32x16& p0, f32x16& p1, float alpha, float& l_reg, bf16x8& pa0, bf16x8& pa1, bf16x8& pa2, bf16x8& pa3) {
;     ...
;     for (int r = 0; r < 16; ++r) p1[r] = __builtin_amdgcn_exp2f(p1[r]);
;     float ps = 0;
; #pragma unroll
;     for (int r = 0; r < 16; ++r) ps += p0[r];
; #pragma unroll
;     for (int r = 0; r < 16; ++r) ps += p1[r];
;     { auto rr = __builtin_amdgcn_permlane32_swap(__float_as_uint(ps), __float_as_uint(ps), false, false);
;       ps = __uint_as_float(rr[0]) + __uint_as_float(rr[1]); }
;     l_reg = l_reg * alpha + ps;
;     ...
;     PK4(p0, 0, pa0); PK4(p0, 8, pa1); PK4(p1, 0, pa2); PK4(p1, 8, pa3);
; template <int VB, bool SK>
; __device__ __forceinline__ void pv_tile(f32x16* o, int vb0, bf16x8 pa0, bf16x8 pa1, bf16x8 pa2, bf16x8 pa3, bool act) {
;     if (SK && !act) return;
;     ...
;     if (ATT_PRIO) __builtin_amdgcn_s_setprio(1);
;     PV_D0(0); PV_D0(1); PV_D0(2); PV_D0(3);
	v_mfma_f32_32x32x16_bf16 v[102:117], v[4:7], v[12:15], v[102:117]
	v_exp_f32_e32 v4, v140
	v_exp_f32_e32 v5, v141
	v_exp_f32_e32 v6, v138
	v_exp_f32_e32 v7, v139
	v_mfma_f32_32x32x16_bf16 v[86:101], v[8:11], v[12:15], v[86:101]
	ds_read_b64_tr_b16 v[232:233], v210 offset:0
	ds_read_b64_tr_b16 v[234:235], v210 offset:0x800
	ds_read_b64_tr_b16 v[236:237], v210 offset:0x1000
	ds_read_b64_tr_b16 v[238:239], v210 offset:0x1800
	ds_read_b64_tr_b16 v[240:241], v210 offset:0x2000
	ds_read_b64_tr_b16 v[242:243], v210 offset:0x2800
	ds_read_b64_tr_b16 v[244:245], v210 offset:0x3000
	ds_read_b64_tr_b16 v[246:247], v210 offset:0x3800
	v_add_f32_e32 v12, v228, v188
	v_add_f32_e32 v12, v186, v12
	v_add_f32_e32 v12, v189, v12
	v_add_f32_e32 v12, v185, v12
	v_add_f32_e32 v12, v187, v12
	v_add_f32_e32 v12, v183, v12
	v_add_f32_e32 v12, v184, v12
	v_add_f32_e32 v12, v179, v12
	v_add_f32_e32 v12, v182, v12
	v_add_f32_e32 v12, v144, v12
	v_add_f32_e32 v12, v180, v12
	v_add_f32_e32 v12, v142, v12
	v_add_f32_e32 v12, v181, v12
	v_add_f32_e32 v12, v143, v12
	v_add_f32_e32 v12, v145, v12
	v_exp_f32_e32 v8, v136
	v_add_f32_e32 v12, v4, v12
	v_exp_f32_e32 v9, v137
	v_add_f32_e32 v12, v5, v12
	v_exp_f32_e32 v10, v134
	v_add_f32_e32 v12, v6, v12
	v_exp_f32_e32 v11, v135
	v_add_f32_e32 v12, v7, v12
	v_add_f32_e32 v12, v8, v12
	v_add_f32_e32 v12, v9, v12
	v_add_f32_e32 v12, v10, v12
	v_add_f32_e32 v12, v11, v12
	v_add_f32_e32 v12, v122, v12
	v_add_f32_e32 v12, v123, v12
	v_add_f32_e32 v12, v124, v12
	v_add_f32_e32 v12, v125, v12
	v_add_f32_e32 v12, v126, v12
	v_add_f32_e32 v12, v127, v12
	v_add_f32_e32 v12, v128, v12
	v_add_f32_e32 v195, v129, v12
	v_mov_b32_e32 v226, v195
	s_nop 1
	v_permlane32_swap_b32_e32 v195, v226
	v_cvt_pk_bf16_f32 v12, v188, v228
	v_cvt_pk_bf16_f32 v13, v186, v189
	v_cvt_pk_bf16_f32 v14, v185, v187
	v_cvt_pk_bf16_f32 v15, v183, v184
	v_cvt_pk_bf16_f32 v82, v179, v182
	v_cvt_pk_bf16_f32 v83, v144, v180
	v_cvt_pk_bf16_f32 v84, v142, v181
	v_cvt_pk_bf16_f32 v85, v143, v145
	v_cvt_pk_bf16_f32 v118, v4, v5
	v_cvt_pk_bf16_f32 v119, v6, v7
	v_cvt_pk_bf16_f32 v120, v8, v9
	v_cvt_pk_bf16_f32 v121, v10, v11
	v_cvt_pk_bf16_f32 v122, v122, v123
	v_cvt_pk_bf16_f32 v123, v124, v125
	v_cvt_pk_bf16_f32 v124, v126, v127
	v_cvt_pk_bf16_f32 v125, v128, v129
	s_nop 0
	v_permlane32_swap_b32_e32 v12, v14
	v_permlane32_swap_b32_e32 v13, v15
	v_permlane32_swap_b32_e32 v82, v84
	v_permlane32_swap_b32_e32 v83, v85
	v_permlane32_swap_b32_e32 v118, v120
	v_permlane32_swap_b32_e32 v119, v121
	v_permlane32_swap_b32_e32 v122, v124
	v_permlane32_swap_b32_e32 v123, v125
	s_add_i32 s10, s48, 0xffffffa0
	s_sub_i32 s72, s48, 64
	s_mov_b32 s73, s11
	s_lshl_b64 s[50:51], s[10:11], 12
	s_lshl_b64 s[72:73], s[72:73], 12
	v_lshl_add_u64 v[4:5], v[196:197], 0, s[50:51]
	v_lshl_add_u64 v[8:9], v[196:197], 0, s[72:73]
	v_lshl_add_u64 v[126:127], v[198:199], 0, s[50:51]
	s_add_i32 m0, s37, 0x8000
	global_load_dwordx4 v[4:7], v[4:5], off
	s_nop 0
	global_load_dwordx4 v[8:11], v[8:9], off
	s_lshl_b64 s[50:51], s[10:11], 7
	global_load_lds_dwordx4 v[126:127], off
	v_lshl_add_u64 v[126:127], v[198:199], 0, s[72:73]
	s_add_i32 m0, s37, 0xa000
	s_nop 0
	global_load_lds_dwordx4 v[126:127], off
	v_lshl_add_u64 v[126:127], v[16:17], 0, s[50:51]
	s_add_i32 m0, s37, 0x10800
	s_nop 0
	global_load_lds_dwordx4 v[126:127], off
	s_waitcnt lgkmcnt(0)
	s_nop 0
	v_mfma_f32_32x32x16_bf16 v[66:81], v[12:15], v[232:235], v[66:81]
	ds_read_b64_tr_b16 v[126:127], v210 offset:0x200
	ds_read_b64_tr_b16 v[128:129], v210 offset:0xa00
	v_mfma_f32_32x32x16_bf16 v[66:81], v[82:85], v[236:239], v[66:81]
	ds_read_b64_tr_b16 v[130:131], v210 offset:0x1200
	ds_read_b64_tr_b16 v[132:133], v210 offset:0x1a00
	v_mfma_f32_32x32x16_bf16 v[66:81], v[118:121], v[240:243], v[66:81]
	ds_read_b64_tr_b16 v[134:135], v210 offset:0x2200
	ds_read_b64_tr_b16 v[136:137], v210 offset:0x2a00
	ds_read_b64_tr_b16 v[142:143], v210 offset:0x3200
	ds_read_b64_tr_b16 v[144:145], v210 offset:0x3a00
	s_waitcnt lgkmcnt(0)
	v_mfma_f32_32x32x16_bf16 v[66:81], v[122:125], v[244:247], v[66:81]
	v_mfma_f32_32x32x16_bf16 v[50:65], v[12:15], v[126:129], v[50:65]
	ds_read_b64_tr_b16 v[126:127], v210 offset:0x400
	ds_read_b64_tr_b16 v[128:129], v210 offset:0xc00
	v_mfma_f32_32x32x16_bf16 v[50:65], v[82:85], v[130:133], v[50:65]
	ds_read_b64_tr_b16 v[130:131], v210 offset:0x1400
	ds_read_b64_tr_b16 v[132:133], v210 offset:0x1c00
	v_mfma_f32_32x32x16_bf16 v[50:65], v[118:121], v[134:137], v[50:65]
	ds_read_b64_tr_b16 v[134:135], v210 offset:0x2400
	ds_read_b64_tr_b16 v[136:137], v210 offset:0x2c00
	ds_read_b64_tr_b16 v[138:139], v210 offset:0x3400
	ds_read_b64_tr_b16 v[140:141], v210 offset:0x3c00
	s_waitcnt lgkmcnt(0)
	v_mfma_f32_32x32x16_bf16 v[50:65], v[122:125], v[142:145], v[50:65]
	v_mfma_f32_32x32x16_bf16 v[34:49], v[12:15], v[126:129], v[34:49]
	ds_read_b64_tr_b16 v[126:127], v210 offset:0x600
	ds_read_b64_tr_b16 v[128:129], v210 offset:0xe00
	v_mfma_f32_32x32x16_bf16 v[34:49], v[82:85], v[130:133], v[34:49]
	ds_read_b64_tr_b16 v[130:131], v210 offset:0x1600
	ds_read_b64_tr_b16 v[132:133], v210 offset:0x1e00
	v_mfma_f32_32x32x16_bf16 v[34:49], v[118:121], v[134:137], v[34:49]
	ds_read_b64_tr_b16 v[134:135], v210 offset:0x2600
	ds_read_b64_tr_b16 v[136:137], v210 offset:0x2e00
	ds_read_b64_tr_b16 v[142:143], v210 offset:0x3600
	ds_read_b64_tr_b16 v[144:145], v210 offset:0x3e00
	s_waitcnt lgkmcnt(0)
	v_mfma_f32_32x32x16_bf16 v[34:49], v[122:125], v[138:141], v[34:49]
	v_mfma_f32_32x32x16_bf16 v[18:33], v[12:15], v[126:129], v[18:33]
	s_cmp_le_i32 s7, s46
	s_cselect_b64 s[50:51], -1, 0
	s_cmp_gt_i32 s6, s18
	s_cselect_b64 s[6:7], -1, 0
	s_and_b64 s[6:7], s[6:7], s[50:51]
	s_and_b64 vcc, exec, s[6:7]
	v_mfma_f32_32x32x16_bf16 v[18:33], v[82:85], v[130:133], v[18:33]
	v_mfma_f32_32x32x16_bf16 v[18:33], v[118:121], v[134:137], v[18:33]
	v_mfma_f32_32x32x16_bf16 v[18:33], v[122:125], v[142:145], v[18:33]
	s_cbranch_vccnz .LBB0_527
; __device__ __forceinline__ void mask_tile(f32x16& p0, f32x16& p1, int dq, unsigned W) {
;     const float NEG = -__builtin_inff();
; #pragma unroll
;     for (int r = 0; r < 16; ++r) {
;         const int c = (r & 3) + 8 * (r >> 2);
;         if ((unsigned)(dq - c) >= W) p0[r] = NEG;
;         if ((unsigned)(dq - c - 32) >= W) p1[r] = NEG;
;     }
; }
	v_add_u32_e32 v12, 0x7b, v193
	v_cmp_gt_u32_e32 vcc, 2.0, v12
	v_add_u32_e32 v12, 0x5b, v193
	s_nop 0
	v_cndmask_b32_e32 v102, v200, v102, vcc
	v_cmp_gt_u32_e32 vcc, 2.0, v12
	v_add_u32_e32 v12, 0x7a, v193
	s_nop 0
	v_cndmask_b32_e32 v86, v200, v86, vcc
	v_cmp_gt_u32_e32 vcc, 2.0, v12
	v_add_u32_e32 v12, 0x5a, v193
	s_nop 0
	v_cndmask_b32_e32 v103, v200, v103, vcc
	v_cmp_gt_u32_e32 vcc, 2.0, v12
	v_add_u32_e32 v12, 0x79, v193
	s_nop 0
	v_cndmask_b32_e32 v87, v200, v87, vcc
	v_cmp_gt_u32_e32 vcc, 2.0, v12
	v_add_u32_e32 v12, 0x59, v193
	s_nop 0
	v_cndmask_b32_e32 v104, v200, v104, vcc
	v_cmp_gt_u32_e32 vcc, 2.0, v12
	v_add_u32_e32 v12, 0x78, v193
	s_nop 0
	v_cndmask_b32_e32 v88, v200, v88, vcc
	v_cmp_gt_u32_e32 vcc, 2.0, v12
	v_add_u32_e32 v12, 0x58, v193
	s_nop 0
	v_cndmask_b32_e32 v105, v200, v105, vcc
	v_cmp_gt_u32_e32 vcc, 2.0, v12
	v_add_u32_e32 v12, 0x73, v193
	s_nop 0
	v_cndmask_b32_e32 v89, v200, v89, vcc
	v_cmp_gt_u32_e32 vcc, 2.0, v12
	v_add_u32_e32 v12, 0x53, v193
	s_nop 0
	v_cndmask_b32_e32 v106, v200, v106, vcc
	v_cmp_gt_u32_e32 vcc, 2.0, v12
	v_add_u32_e32 v12, 0x72, v193
	s_nop 0
	v_cndmask_b32_e32 v90, v200, v90, vcc
	v_cmp_gt_u32_e32 vcc, 2.0, v12
	v_add_u32_e32 v12, 0x52, v193
	s_nop 0
	v_cndmask_b32_e32 v107, v200, v107, vcc
	v_cmp_gt_u32_e32 vcc, 2.0, v12
	v_add_u32_e32 v12, 0x71, v193
	s_nop 0
	v_cndmask_b32_e32 v91, v200, v91, vcc
	v_cmp_gt_u32_e32 vcc, 2.0, v12
	v_add_u32_e32 v12, 0x51, v193
	s_nop 0
	v_cndmask_b32_e32 v108, v200, v108, vcc
	v_cmp_gt_u32_e32 vcc, 2.0, v12
	v_add_u32_e32 v12, 0x70, v193
	s_nop 0
	v_cndmask_b32_e32 v92, v200, v92, vcc
	v_cmp_gt_u32_e32 vcc, 2.0, v12
	v_add_u32_e32 v12, 0x50, v193
	s_nop 0
	v_cndmask_b32_e32 v109, v200, v109, vcc
	v_cmp_gt_u32_e32 vcc, 2.0, v12
	v_add_u32_e32 v12, 0x6b, v193
	s_nop 0
	v_cndmask_b32_e32 v93, v200, v93, vcc
	v_cmp_gt_u32_e32 vcc, 2.0, v12
	v_add_u32_e32 v12, 0x4b, v193
	s_nop 0
	v_cndmask_b32_e32 v110, v200, v110, vcc
	v_cmp_gt_u32_e32 vcc, 2.0, v12
	v_add_u32_e32 v12, 0x6a, v193
	s_nop 0
	v_cndmask_b32_e32 v94, v200, v94, vcc
	v_cmp_gt_u32_e32 vcc, 2.0, v12
	v_add_u32_e32 v12, 0x4a, v193
	s_nop 0
	v_cndmask_b32_e32 v111, v200, v111, vcc
	v_cmp_gt_u32_e32 vcc, 2.0, v12
	v_add_u32_e32 v12, 0x69, v193
	s_nop 0
	v_cndmask_b32_e32 v95, v200, v95, vcc
	v_cmp_gt_u32_e32 vcc, 2.0, v12
	v_add_u32_e32 v12, 0x49, v193
	s_nop 0
	v_cndmask_b32_e32 v112, v200, v112, vcc
	v_cmp_gt_u32_e32 vcc, 2.0, v12
	v_add_u32_e32 v12, 0x68, v193
	s_nop 0
	v_cndmask_b32_e32 v96, v200, v96, vcc
	v_cmp_gt_u32_e32 vcc, 2.0, v12
	v_add_u32_e32 v12, 0x48, v193
	s_nop 0
	v_cndmask_b32_e32 v113, v200, v113, vcc
	v_cmp_gt_u32_e32 vcc, 2.0, v12
	v_add_u32_e32 v12, 0x63, v193
	s_nop 0
	v_cndmask_b32_e32 v97, v200, v97, vcc
	v_cmp_gt_u32_e32 vcc, 2.0, v12
	v_add_u32_e32 v12, 0x43, v193
	s_nop 0
	v_cndmask_b32_e32 v114, v200, v114, vcc
	v_cmp_gt_u32_e32 vcc, 2.0, v12
	v_add_u32_e32 v12, 0x62, v193
	s_nop 0
	v_cndmask_b32_e32 v98, v200, v98, vcc
	v_cmp_gt_u32_e32 vcc, 2.0, v12
	v_add_u32_e32 v12, 0x42, v193
	s_nop 0
	v_cndmask_b32_e32 v115, v200, v115, vcc
	v_cmp_gt_u32_e32 vcc, 2.0, v12
	v_add_u32_e32 v12, 0x61, v193
	s_nop 0
	v_cndmask_b32_e32 v99, v200, v99, vcc
	v_cmp_gt_u32_e32 vcc, 2.0, v12
	v_add_u32_e32 v12, 0x41, v193
	s_nop 0
	v_cndmask_b32_e32 v116, v200, v116, vcc
	v_cmp_gt_u32_e32 vcc, 2.0, v12
	v_add_u32_e32 v12, 0x60, v193
	s_nop 0
	v_cndmask_b32_e32 v100, v200, v100, vcc
	v_cmp_gt_u32_e32 vcc, 2.0, v12
	v_add_u32_e32 v12, 64, v193
	s_nop 0
	v_cndmask_b32_e32 v117, v200, v117, vcc
	v_cmp_gt_u32_e32 vcc, 2.0, v12
	s_nop 1
	v_cndmask_b32_e32 v101, v200, v101, vcc

; template <int MODE>
; __device__ __forceinline__ void partialSM(f32x16& p0, f32x16& p1, float& m_reg, float& mn, float& alpha) {
;     ...
;     constexpr float C2 = 1.4426950408889634f * SCALE;
;     if (__builtin_expect(__all((pmax - m_reg) * SCALE <= THR), 1)) { mn = m_reg; alpha = 1.f; }
;     else { mn = fmaxf(m_reg, pmax); alpha = __builtin_amdgcn_exp2f((m_reg - mn) * C2); m_reg = mn; }
;     const float mnL = -mn * C2;
; #pragma unroll
;     for (int r = 0; r < 16; ++r) p0[r] = fmaf(p0[r], C2, mnL);
; #pragma unroll
;     for (int r = 0; r < 16; ++r) p1[r] = fmaf(p1[r], C2, mnL);
; #pragma unroll
;     for (int r = 0; r < 16; ++r) p0[r] = __builtin_amdgcn_exp2f(p0[r]);
; template <int KB, bool SK, bool ROPE, bool QHALF>
; __device__ __forceinline__ void qkt(f32x16& p0, f32x16& p1, const char* lds, int r32, int hi, const bf16x8* qr, const char* qrl, bool act) {
;     ...
;     const char* kb[4];
; #pragma unroll
;     for (int dd = 0; dd < 4; ++dd) kb[dd] = lds + OFF_K + KB * SHM_K + KSWZ(r32, (dd * 16 + hi * 8) * 2);
; #pragma unroll
;     for (int d0 = 0; d0 < 8; ++d0) { const char* a = kb[d0 & 3] + (d0 >> 2) * 128;
;         bf16x8 b0 = *reinterpret_cast<const bf16x8*>(a);
;         bf16x8 b1 = *reinterpret_cast<const bf16x8*>(a + 32 * 256);
;         bf16x8 qf;
;         if constexpr (QHALF) { if (d0 >= 4) qf = *reinterpret_cast<const bf16x8*>(qrl + (d0 - 4) * 1024); else qf = qr[d0]; } else qf = qr[d0];
;         p0 = __builtin_amdgcn_mfma_f32_32x32x16_bf16(b0, qf, p0, 0, 0, 0);
;         p1 = __builtin_amdgcn_mfma_f32_32x32x16_bf16(b1, qf, p1, 0, 0, 0); }
.LBB0_531:
	v_cndmask_b32_e64 v228, v12, v178, s[6:7]
	v_mul_f32_e32 v12, 0xbdd53b94, v228
	v_fmamk_f32 v82, v102, 0x3dd53b94, v12
	v_fmamk_f32 v83, v103, 0x3dd53b94, v12
	v_fmamk_f32 v84, v104, 0x3dd53b94, v12
	v_fmamk_f32 v85, v105, 0x3dd53b94, v12
	v_fmamk_f32 v118, v106, 0x3dd53b94, v12
	v_fmamk_f32 v119, v107, 0x3dd53b94, v12
	v_fmamk_f32 v120, v108, 0x3dd53b94, v12
	v_fmamk_f32 v121, v109, 0x3dd53b94, v12
	v_fmamk_f32 v122, v110, 0x3dd53b94, v12
	v_fmamk_f32 v123, v111, 0x3dd53b94, v12
	v_fmamk_f32 v112, v112, 0x3dd53b94, v12
	v_fmamk_f32 v113, v113, 0x3dd53b94, v12
	v_fmamk_f32 v114, v114, 0x3dd53b94, v12
	v_fmamk_f32 v115, v115, 0x3dd53b94, v12
	v_fmamk_f32 v116, v116, 0x3dd53b94, v12
	v_fmamk_f32 v117, v117, 0x3dd53b94, v12
	v_fmamk_f32 v102, v86, 0x3dd53b94, v12
	v_fmamk_f32 v103, v87, 0x3dd53b94, v12
	v_fmamk_f32 v104, v88, 0x3dd53b94, v12
	v_fmamk_f32 v110, v89, 0x3dd53b94, v12
	v_fmamk_f32 v111, v90, 0x3dd53b94, v12
	v_fmamk_f32 v14, v91, 0x3dd53b94, v12
	v_fmamk_f32 v15, v92, 0x3dd53b94, v12
	v_fmamk_f32 v105, v93, 0x3dd53b94, v12
	v_fmamk_f32 v106, v94, 0x3dd53b94, v12
	v_fmamk_f32 v107, v95, 0x3dd53b94, v12
	v_fmamk_f32 v108, v96, 0x3dd53b94, v12
	v_fmamk_f32 v109, v97, 0x3dd53b94, v12
	v_exp_f32_e32 v82, v82
	v_exp_f32_e32 v83, v83
	v_exp_f32_e32 v84, v84
	v_exp_f32_e32 v85, v85
	v_exp_f32_e32 v86, v118
	v_exp_f32_e32 v87, v119
	v_exp_f32_e32 v88, v120
	v_exp_f32_e32 v89, v121
	v_exp_f32_e32 v90, v122
	v_exp_f32_e32 v91, v123
	v_exp_f32_e32 v92, v112
	v_exp_f32_e32 v93, v113
	v_exp_f32_e32 v94, v114
	v_exp_f32_e32 v95, v115
	v_exp_f32_e32 v96, v116
	v_exp_f32_e32 v97, v117
	v_fmamk_f32 v13, v98, 0x3dd53b94, v12
	v_fmamk_f32 v112, v99, 0x3dd53b94, v12
	v_fmamk_f32 v113, v100, 0x3dd53b94, v12
	v_fmac_f32_e32 v12, 0x3dd53b94, v101
	s_waitcnt lgkmcnt(0)
	ds_read_b128 v[98:101], v213 offset:32768
	ds_read_b128 v[114:117], v213 offset:40960
	v_exp_f32_e32 v105, v105
	v_exp_f32_e32 v106, v106
	v_exp_f32_e32 v107, v107
	s_waitcnt lgkmcnt(1)
	v_mfma_f32_32x32x16_bf16 v[130:145], v[98:101], v[174:177], 0
	ds_read_b128 v[98:101], v214 offset:32768
	ds_read_b128 v[178:181], v214 offset:40960
	v_exp_f32_e32 v108, v108
	v_exp_f32_e32 v109, v109
	s_waitcnt lgkmcnt(2)
	v_mfma_f32_32x32x16_bf16 v[114:129], v[114:117], v[174:177], 0
	s_waitcnt lgkmcnt(1)
	v_mfma_f32_32x32x16_bf16 v[130:145], v[98:101], v[170:173], v[130:145]
	s_waitcnt lgkmcnt(0)
	v_mfma_f32_32x32x16_bf16 v[114:129], v[178:181], v[170:173], v[114:129]
	ds_read_b128 v[98:101], v215 offset:32768
	ds_read_b128 v[178:181], v215 offset:40960
	s_waitcnt lgkmcnt(1)
	v_mfma_f32_32x32x16_bf16 v[130:145], v[98:101], v[166:169], v[130:145]
	s_waitcnt lgkmcnt(0)
	v_mfma_f32_32x32x16_bf16 v[114:129], v[178:181], v[166:169], v[114:129]
	ds_read_b128 v[98:101], v216 offset:32768
	ds_read_b128 v[178:181], v216 offset:40960
	s_waitcnt lgkmcnt(1)
	v_mfma_f32_32x32x16_bf16 v[130:145], v[98:101], v[162:165], v[130:145]
	s_waitcnt lgkmcnt(0)
	v_mfma_f32_32x32x16_bf16 v[114:129], v[178:181], v[162:165], v[114:129]
	ds_read_b128 v[98:101], v213 offset:32896
	ds_read_b128 v[178:181], v213 offset:41088
	s_waitcnt lgkmcnt(1)
	v_mfma_f32_32x32x16_bf16 v[130:145], v[98:101], v[158:161], v[130:145]
	s_waitcnt lgkmcnt(0)
	v_mfma_f32_32x32x16_bf16 v[114:129], v[178:181], v[158:161], v[114:129]
	ds_read_b128 v[98:101], v214 offset:32896
	ds_read_b128 v[178:181], v214 offset:41088
	s_waitcnt lgkmcnt(1)
	v_mfma_f32_32x32x16_bf16 v[130:145], v[98:101], v[154:157], v[130:145]
	s_waitcnt lgkmcnt(0)
	v_mfma_f32_32x32x16_bf16 v[114:129], v[178:181], v[154:157], v[114:129]
	ds_read_b128 v[98:101], v215 offset:32896
	ds_read_b128 v[178:181], v215 offset:41088
	s_waitcnt lgkmcnt(1)
	v_mfma_f32_32x32x16_bf16 v[130:145], v[98:101], v[150:153], v[130:145]
	s_waitcnt lgkmcnt(0)
	v_mfma_f32_32x32x16_bf16 v[114:129], v[178:181], v[150:153], v[114:129]
	ds_read_b128 v[98:101], v216 offset:32896
	ds_read_b128 v[178:181], v216 offset:41088
	s_waitcnt lgkmcnt(1)
	v_mfma_f32_32x32x16_bf16 v[130:145], v[98:101], v[146:149], v[130:145]
	s_waitcnt lgkmcnt(0)
	v_mfma_f32_32x32x16_bf16 v[114:129], v[178:181], v[146:149], v[114:129]
	ds_read_b128 v[98:101], v222
	ds_read_b128 v[178:181], v222 offset:4096
	ds_read_b128 v[182:185], v202
	s_waitcnt lgkmcnt(0)
; __device__ __forceinline__ void finishSM(f32x16& p0, f32x16& p1, float alpha, float& l_reg, bf16x8& pa0, bf16x8& pa1, bf16x8& pa2, bf16x8& pa3) {
;     ...
;     for (int r = 0; r < 16; ++r) p1[r] = __builtin_amdgcn_exp2f(p1[r]);
;     float ps = 0;
; #pragma unroll
;     for (int r = 0; r < 16; ++r) ps += p0[r];
; #pragma unroll
;     for (int r = 0; r < 16; ++r) ps += p1[r];
;     { auto rr = __builtin_amdgcn_permlane32_swap(__float_as_uint(ps), __float_as_uint(ps), false, false);
;       ps = __uint_as_float(rr[0]) + __uint_as_float(rr[1]); }
;     l_reg = l_reg * alpha + ps;
;     ...
;     PK4(p0, 0, pa0); PK4(p0, 8, pa1); PK4(p1, 0, pa2); PK4(p1, 8, pa3);
	v_mfma_f32_32x32x16_bf16 v[130:145], v[98:101], v[182:185], v[130:145]
	v_mfma_f32_32x32x16_bf16 v[114:129], v[178:181], v[182:185], v[114:129]
	ds_read_b128 v[98:101], v223
	ds_read_b128 v[178:181], v223 offset:4096
	ds_read_b128 v[182:185], v202 offset:1024
	s_waitcnt lgkmcnt(0)
	v_mfma_f32_32x32x16_bf16 v[130:145], v[98:101], v[182:185], v[130:145]
	v_mfma_f32_32x32x16_bf16 v[114:129], v[178:181], v[182:185], v[114:129]
	ds_read_b128 v[98:101], v224
	ds_read_b128 v[178:181], v224 offset:4096
	ds_read_b128 v[182:185], v202 offset:2048
	s_waitcnt lgkmcnt(0)
	v_mfma_f32_32x32x16_bf16 v[130:145], v[98:101], v[182:185], v[130:145]
	v_mfma_f32_32x32x16_bf16 v[114:129], v[178:181], v[182:185], v[114:129]
	ds_read_b128 v[98:101], v225
	ds_read_b128 v[178:181], v225 offset:4096
	ds_read_b128 v[182:185], v202 offset:3072
	s_waitcnt lgkmcnt(0)
	v_mfma_f32_32x32x16_bf16 v[130:145], v[98:101], v[182:185], v[130:145]
	ds_read_b64_tr_b16 v[232:233], v210 offset:0x4000
	ds_read_b64_tr_b16 v[234:235], v210 offset:0x4800
	ds_read_b64_tr_b16 v[236:237], v210 offset:0x5000
	ds_read_b64_tr_b16 v[238:239], v210 offset:0x5800
	ds_read_b64_tr_b16 v[240:241], v210 offset:0x6000
	ds_read_b64_tr_b16 v[242:243], v210 offset:0x6800
	ds_read_b64_tr_b16 v[244:245], v210 offset:0x7000
	ds_read_b64_tr_b16 v[246:247], v210 offset:0x7800
	v_exp_f32_e32 v98, v102
	v_exp_f32_e32 v102, v111
	v_exp_f32_e32 v111, v112
	v_exp_f32_e32 v112, v113
	v_exp_f32_e32 v113, v12
	v_add_f32_e32 v12, v83, v82
	v_add_f32_e32 v12, v84, v12
	v_add_f32_e32 v12, v85, v12
	v_add_f32_e32 v12, v86, v12
	v_add_f32_e32 v12, v87, v12
	v_add_f32_e32 v12, v88, v12
	v_add_f32_e32 v12, v89, v12
	v_add_f32_e32 v12, v90, v12
	v_add_f32_e32 v12, v91, v12
	v_add_f32_e32 v12, v92, v12
	v_add_f32_e32 v12, v93, v12
	v_add_f32_e32 v12, v94, v12
	v_exp_f32_e32 v99, v103
	v_add_f32_e32 v12, v95, v12
	v_exp_f32_e32 v100, v104
	v_add_f32_e32 v12, v96, v12
	v_exp_f32_e32 v101, v110
	v_add_f32_e32 v12, v97, v12
	v_add_f32_e32 v12, v98, v12
	v_exp_f32_e32 v103, v14
	v_add_f32_e32 v12, v99, v12
	v_exp_f32_e32 v104, v15
	v_add_f32_e32 v12, v100, v12
	v_add_f32_e32 v12, v101, v12
	v_add_f32_e32 v12, v102, v12
	v_add_f32_e32 v12, v103, v12
	v_add_f32_e32 v12, v104, v12
	v_add_f32_e32 v12, v105, v12
	v_exp_f32_e32 v110, v13
	v_add_f32_e32 v12, v106, v12
	v_add_f32_e32 v12, v107, v12
	v_mfma_f32_32x32x16_bf16 v[114:129], v[178:181], v[182:185], v[114:129]
	v_add_f32_e32 v12, v108, v12
	v_add_f32_e32 v12, v109, v12
	v_add_f32_e32 v12, v110, v12
	v_add_f32_e32 v12, v111, v12
	v_add_f32_e32 v12, v112, v12
	v_add_f32_e32 v229, v113, v12
	v_mov_b32_e32 v230, v229
	v_cvt_pk_bf16_f32 v12, v82, v83
	v_cvt_pk_bf16_f32 v13, v84, v85
	v_cvt_pk_bf16_f32 v14, v86, v87
	v_cvt_pk_bf16_f32 v15, v88, v89
	v_cvt_pk_bf16_f32 v178, v90, v91
	v_cvt_pk_bf16_f32 v179, v92, v93
	v_cvt_pk_bf16_f32 v180, v94, v95
	v_cvt_pk_bf16_f32 v181, v96, v97
	v_cvt_pk_bf16_f32 v182, v98, v99
	v_cvt_pk_bf16_f32 v183, v100, v101
	v_cvt_pk_bf16_f32 v184, v102, v103
	v_cvt_pk_bf16_f32 v185, v104, v105
	v_cvt_pk_bf16_f32 v186, v106, v107
	v_cvt_pk_bf16_f32 v187, v108, v109
	v_cvt_pk_bf16_f32 v188, v110, v111
	v_cvt_pk_bf16_f32 v189, v112, v113
	s_nop 1
	v_permlane32_swap_b32_e32 v229, v230
	v_permlane32_swap_b32_e32 v12, v14
	v_permlane32_swap_b32_e32 v13, v15
	v_permlane32_swap_b32_e32 v178, v180
	v_permlane32_swap_b32_e32 v179, v181
	v_permlane32_swap_b32_e32 v182, v184
	v_permlane32_swap_b32_e32 v183, v185
	v_permlane32_swap_b32_e32 v186, v188
	v_permlane32_swap_b32_e32 v187, v189
	s_add_i32 s6, s36, 1
	s_cmp_lt_i32 s6, s71
	s_cselect_b64 s[50:51], -1, 0
	s_cmp_ge_i32 s6, s71
	s_cbranch_scc1 .LBB0_533
	s_sub_i32 s6, s48, 32
	s_mov_b32 s7, s11
	s_mov_b32 s49, s11
	s_lshl_b64 s[72:73], s[6:7], 12
	s_lshl_b64 s[74:75], s[48:49], 12
	v_lshl_add_u64 v[4:5], v[196:197], 0, s[72:73]
	v_lshl_add_u64 v[8:9], v[196:197], 0, s[74:75]
	v_lshl_add_u64 v[248:249], v[198:199], 0, s[72:73]
	s_add_i32 m0, s37, 0xc000
	global_load_dwordx4 v[4:7], v[4:5], off
	s_nop 0
	global_load_dwordx4 v[8:11], v[8:9], off
	s_lshl_b64 s[6:7], s[6:7], 7
	global_load_lds_dwordx4 v[248:249], off
	v_lshl_add_u64 v[248:249], v[198:199], 0, s[74:75]
	s_add_i32 m0, s37, 0xe000
	s_nop 0
	global_load_lds_dwordx4 v[248:249], off
	v_lshl_add_u64 v[248:249], v[16:17], 0, s[6:7]
	s_add_i32 m0, s37, 0x12800
	s_nop 0
	global_load_lds_dwordx4 v[248:249], off

; #define SBAR() __builtin_amdgcn_sched_barrier(0)
; #define ACT(t) (KBASE(t) <= qlo + QBLK - 1 && KBASE(t) + KVBLK - 1 >= qlo - W + 1)
; #define ACT(t) (KBASE(t) <= qlo + QBLK - 1 && KBASE(t) + KVBLK - 1 >= qlo - W + 1)
; #define ACT(t) (KBASE(t) <= qlo + QBLK - 1 && KBASE(t) + KVBLK - 1 >= qlo - W + 1)
; __device__ __forceinline__ void finishSM(f32x16& p0, f32x16& p1, float alpha, float& l_reg, bf16x8& pa0, bf16x8& pa1, bf16x8& pa2, bf16x8& pa3) {
;     ...
;     for (int r = 0; r < 16; ++r) p1[r] = __builtin_amdgcn_exp2f(p1[r]);
;     float ps = 0;
; #pragma unroll
;     for (int r = 0; r < 16; ++r) ps += p0[r];
; #pragma unroll
;     for (int r = 0; r < 16; ++r) ps += p1[r];
;     { auto rr = __builtin_amdgcn_permlane32_swap(__float_as_uint(ps), __float_as_uint(ps), false, false);
;       ps = __uint_as_float(rr[0]) + __uint_as_float(rr[1]); }
;     l_reg = l_reg * alpha + ps;
;     ...
;     PK4(p0, 0, pa0); PK4(p0, 8, pa1); PK4(p1, 0, pa2); PK4(p1, 8, pa3);
; template <int MODE>
; __device__ __forceinline__ void attn_block_pipe(const BlockRef& cur, const BlockRef& nxt, char* lds, LAS unsigned char* ldsl, Seam<MODE>& S) {
;     ...
;     SLOAD_H(nxt, kbn, 0); SBAR();
;     QLOAD(nxt);
;     SBAR();
;     finishSM(pA0, pA1, alA, l_reg, pa0, pa1, pa2, pa3); SBAR();
;     PPV<0, SK>(o, vb0, pa0, pa1, pa2, pa3, ACT(even ? NT - 2 : NT - 1));
.LBB0_543:
	s_add_i32 s6, s69, 0xc0000001
	s_and_b32 s6, s6, 0xffffff00
	s_cmp_gt_i32 s69, 0x3fffffff
	s_cselect_b32 s10, s6, 0
	s_lshl_b64 s[6:7], s[10:11], 12
	s_add_u32 s36, s40, s6
	s_addc_u32 s37, s41, s7
	s_or_b32 s48, s10, 32
	s_mov_b32 s49, s11
	s_lshl_b64 s[48:49], s[48:49], 12
	s_add_u32 s50, s40, s48
	s_addc_u32 s51, s41, s49
	s_lshl_b32 s19, s19, 10
	s_add_i32 s19, s19, 0
	s_add_i32 m0, s19, 0x8000
	s_add_u32 s6, s38, s6
	s_addc_u32 s7, s39, s7
	global_load_dwordx4 v[114:117], v194, s[36:37]
	global_load_dwordx4 v[118:121], v194, s[50:51]
	s_nop 0
	global_load_lds_dwordx4 v192, s[6:7]
	s_add_i32 m0, s19, 0xa000
	s_add_u32 s6, s38, s48
	s_addc_u32 s7, s39, s49
	global_load_lds_dwordx4 v192, s[6:7]
	s_add_i32 m0, s19, 0x10800
	s_lshl_b64 s[6:7], s[10:11], 7
	s_add_u32 s6, s8, s6
	s_addc_u32 s7, s9, s7
	global_load_lds_dwordx4 v190, s[6:7]
	s_add_i32 s6, s70, s69
	s_mul_i32 s19, s6, 0xc00
	v_mul_u32_u24_e32 v2, 0xc00, v205
	s_mul_hi_i32 s10, s6, 0xc00
	s_add_u32 s6, s63, s19
	v_or_b32_e32 v2, v212, v2
	s_addc_u32 s7, s65, s10
	global_load_dwordx4 v[174:177], v2, s[6:7]
	global_load_dwordx4 v[170:173], v2, s[6:7] offset:32
	global_load_dwordx4 v[166:169], v2, s[6:7] offset:64
	global_load_dwordx4 v[162:165], v2, s[6:7] offset:96
	global_load_dwordx4 v[158:161], v2, s[6:7] offset:128
	global_load_dwordx4 v[154:157], v2, s[6:7] offset:160
	global_load_dwordx4 v[150:153], v2, s[6:7] offset:192
	global_load_dwordx4 v[146:149], v2, s[6:7] offset:224
	s_add_u32 s6, s61, s19
	s_addc_u32 s7, s64, s10
	global_load_dwordx4 v[4:7], v2, s[6:7]
	global_load_dwordx4 v[8:11], v2, s[6:7] offset:32
	global_load_dwordx4 v[12:15], v2, s[6:7] offset:64
	global_load_dwordx4 v[122:125], v2, s[6:7] offset:96
	v_add_f32_e32 v2, v228, v188
	v_add_f32_e32 v2, v186, v2
	v_add_f32_e32 v2, v189, v2
	v_add_f32_e32 v2, v185, v2
	v_add_f32_e32 v2, v187, v2
	v_add_f32_e32 v2, v183, v2
	v_add_f32_e32 v2, v184, v2
	v_add_f32_e32 v2, v179, v2
	v_add_f32_e32 v2, v182, v2
	v_add_f32_e32 v2, v144, v2
	v_add_f32_e32 v2, v180, v2
	v_exp_f32_e32 v16, v140
	v_add_f32_e32 v2, v142, v2
	v_exp_f32_e32 v17, v141
	v_add_f32_e32 v2, v181, v2
	v_exp_f32_e32 v138, v138
	v_add_f32_e32 v2, v143, v2
	v_exp_f32_e32 v139, v139
	v_add_f32_e32 v2, v145, v2
	v_exp_f32_e32 v136, v136
	v_add_f32_e32 v2, v16, v2
	v_exp_f32_e32 v137, v137
	v_add_f32_e32 v2, v17, v2
	v_exp_f32_e32 v140, v134
	v_add_f32_e32 v2, v138, v2
	v_exp_f32_e32 v141, v135
	v_add_f32_e32 v2, v139, v2
	v_exp_f32_e32 v190, v132
	v_add_f32_e32 v2, v136, v2
	v_exp_f32_e32 v192, v133
	v_add_f32_e32 v2, v137, v2
	v_exp_f32_e32 v193, v130
	v_add_f32_e32 v2, v140, v2
	v_exp_f32_e32 v194, v131
	v_add_f32_e32 v2, v141, v2
	v_exp_f32_e32 v195, v126
	v_add_f32_e32 v2, v190, v2
	v_exp_f32_e32 v196, v127
	v_add_f32_e32 v2, v192, v2
	v_exp_f32_e32 v197, v128
	v_add_f32_e32 v2, v193, v2
	v_exp_f32_e32 v198, v129
	v_add_f32_e32 v2, v194, v2
	v_add_f32_e32 v2, v195, v2
	v_add_f32_e32 v2, v196, v2
	v_add_f32_e32 v2, v197, v2
	v_add_f32_e32 v2, v198, v2
	v_mov_b32_e32 v126, v2
	s_nop 1
	v_permlane32_swap_b32_e32 v2, v126
	v_add_f32_e32 v2, v2, v126
	v_fmac_f32_e32 v2, v191, v221
	v_cvt_pk_bf16_f32 v126, v188, v228
	v_cvt_pk_bf16_f32 v127, v186, v189
	v_cvt_pk_bf16_f32 v128, v185, v187
	v_cvt_pk_bf16_f32 v129, v183, v184
	v_cvt_pk_bf16_f32 v130, v179, v182
	v_cvt_pk_bf16_f32 v131, v144, v180
	v_cvt_pk_bf16_f32 v132, v142, v181
	v_cvt_pk_bf16_f32 v133, v143, v145
	v_cvt_pk_bf16_f32 v134, v16, v17
	v_cvt_pk_bf16_f32 v135, v138, v139
	v_cvt_pk_bf16_f32 v136, v136, v137
	v_cvt_pk_bf16_f32 v137, v140, v141
	v_cvt_pk_bf16_f32 v138, v190, v192
	v_cvt_pk_bf16_f32 v139, v193, v194
	v_cvt_pk_bf16_f32 v140, v195, v196
	v_cvt_pk_bf16_f32 v141, v197, v198
	s_nop 0
	v_permlane32_swap_b32_e32 v126, v128
	v_permlane32_swap_b32_e32 v127, v129
	v_permlane32_swap_b32_e32 v130, v132
	v_permlane32_swap_b32_e32 v131, v133
	v_permlane32_swap_b32_e32 v134, v136
	v_permlane32_swap_b32_e32 v135, v137
	v_permlane32_swap_b32_e32 v138, v140
	v_permlane32_swap_b32_e32 v139, v141
	ds_read_b64_tr_b16 v[142:143], v210 offset:0
	ds_read_b64_tr_b16 v[144:145], v210 offset:0x800
	ds_read_b64_tr_b16 v[180:181], v210 offset:0x1000
	ds_read_b64_tr_b16 v[182:183], v210 offset:0x1800
	ds_read_b64_tr_b16 v[184:185], v210 offset:0x2000
	ds_read_b64_tr_b16 v[186:187], v210 offset:0x2800
	ds_read_b64_tr_b16 v[188:189], v210 offset:0x3000
	ds_read_b64_tr_b16 v[190:191], v210 offset:0x3800
	s_waitcnt lgkmcnt(0)
	s_nop 0
	v_mfma_f32_32x32x16_bf16 v[66:81], v[126:129], v[142:145], v[66:81]
	ds_read_b64_tr_b16 v[142:143], v210 offset:0x200
	ds_read_b64_tr_b16 v[144:145], v210 offset:0xa00
	v_mfma_f32_32x32x16_bf16 v[66:81], v[130:133], v[180:183], v[66:81]
	ds_read_b64_tr_b16 v[180:181], v210 offset:0x1200
	ds_read_b64_tr_b16 v[182:183], v210 offset:0x1a00
	v_mfma_f32_32x32x16_bf16 v[66:81], v[134:137], v[184:187], v[66:81]
	ds_read_b64_tr_b16 v[184:185], v210 offset:0x2200
	ds_read_b64_tr_b16 v[186:187], v210 offset:0x2a00
	ds_read_b64_tr_b16 v[192:193], v210 offset:0x3200
	ds_read_b64_tr_b16 v[194:195], v210 offset:0x3a00
	s_waitcnt lgkmcnt(0)
	v_mfma_f32_32x32x16_bf16 v[66:81], v[138:141], v[188:191], v[66:81]
	v_mfma_f32_32x32x16_bf16 v[50:65], v[126:129], v[142:145], v[50:65]
	ds_read_b64_tr_b16 v[142:143], v210 offset:0x400
	ds_read_b64_tr_b16 v[144:145], v210 offset:0xc00
	v_mfma_f32_32x32x16_bf16 v[50:65], v[130:133], v[180:183], v[50:65]
	ds_read_b64_tr_b16 v[180:181], v210 offset:0x1400
	ds_read_b64_tr_b16 v[182:183], v210 offset:0x1c00
	v_mfma_f32_32x32x16_bf16 v[50:65], v[134:137], v[184:187], v[50:65]
	ds_read_b64_tr_b16 v[184:185], v210 offset:0x2400
	ds_read_b64_tr_b16 v[186:187], v210 offset:0x2c00
	ds_read_b64_tr_b16 v[188:189], v210 offset:0x3400
	ds_read_b64_tr_b16 v[190:191], v210 offset:0x3c00
	s_waitcnt lgkmcnt(0)
	v_mfma_f32_32x32x16_bf16 v[50:65], v[138:141], v[192:195], v[50:65]
	v_mfma_f32_32x32x16_bf16 v[34:49], v[126:129], v[142:145], v[34:49]
	ds_read_b64_tr_b16 v[142:143], v210 offset:0x600
	ds_read_b64_tr_b16 v[144:145], v210 offset:0xe00
	v_mfma_f32_32x32x16_bf16 v[34:49], v[130:133], v[180:183], v[34:49]
	ds_read_b64_tr_b16 v[180:181], v210 offset:0x1600
	ds_read_b64_tr_b16 v[182:183], v210 offset:0x1e00
	v_mfma_f32_32x32x16_bf16 v[34:49], v[134:137], v[184:187], v[34:49]
	ds_read_b64_tr_b16 v[184:185], v210 offset:0x2600
	ds_read_b64_tr_b16 v[186:187], v210 offset:0x2e00
	ds_read_b64_tr_b16 v[192:193], v210 offset:0x3600
	ds_read_b64_tr_b16 v[194:195], v210 offset:0x3e00
	s_waitcnt lgkmcnt(0)
	v_mfma_f32_32x32x16_bf16 v[34:49], v[138:141], v[188:191], v[34:49]
	v_mfma_f32_32x32x16_bf16 v[18:33], v[126:129], v[142:145], v[18:33]
	s_andn2_b64 vcc, exec, s[4:5]
	v_mfma_f32_32x32x16_bf16 v[18:33], v[130:133], v[180:183], v[18:33]
	v_mfma_f32_32x32x16_bf16 v[18:33], v[134:137], v[184:187], v[18:33]
	v_mfma_f32_32x32x16_bf16 v[18:33], v[138:141], v[192:195], v[18:33]
	s_cbranch_vccnz .LBB0_551
; __device__ __forceinline__ void mask_tile(f32x16& p0, f32x16& p1, int dq, unsigned W) {
;     const float NEG = -__builtin_inff();
; #pragma unroll
;     for (int r = 0; r < 16; ++r) {
;         const int c = (r & 3) + 8 * (r >> 2);
;         if ((unsigned)(dq - c) >= W) p0[r] = NEG;
;         if ((unsigned)(dq - c - 32) >= W) p1[r] = NEG;
;     }
; }
	s_lshl_b32 s5, s47, 6
	s_sub_i32 s4, s5, 64
	s_add_i32 s5, s5, -1
	s_cmp_le_i32 s5, s46
	s_cselect_b64 s[6:7], -1, 0
	s_cmp_gt_i32 s4, s18
	s_cselect_b64 s[18:19], -1, 0
	s_and_b64 s[6:7], s[6:7], s[18:19]
	s_and_b64 vcc, exec, s[6:7]
	s_cbranch_vccnz .LBB0_546
	v_subrev_u32_e32 v16, s4, v211
	v_cmp_gt_u32_e32 vcc, 2.0, v16
	v_subrev_u32_e32 v17, 32, v16
	s_nop 0
	v_cndmask_b32_e32 v82, v200, v82, vcc
	v_cmp_gt_u32_e32 vcc, 2.0, v17
	v_add_u32_e32 v17, -1, v16
	s_nop 0
	v_cndmask_b32_e32 v98, v200, v98, vcc
	v_cmp_gt_u32_e32 vcc, 2.0, v17
	v_subrev_u32_e32 v17, 33, v16
	s_nop 0
	v_cndmask_b32_e32 v83, v200, v83, vcc
	v_cmp_gt_u32_e32 vcc, 2.0, v17
	v_add_u32_e32 v17, -2, v16
	s_nop 0
	v_cndmask_b32_e32 v99, v200, v99, vcc
	v_cmp_gt_u32_e32 vcc, 2.0, v17
	v_subrev_u32_e32 v17, 34, v16
	s_nop 0
	v_cndmask_b32_e32 v84, v200, v84, vcc
	v_cmp_gt_u32_e32 vcc, 2.0, v17
	v_add_u32_e32 v17, -3, v16
	s_nop 0
	v_cndmask_b32_e32 v100, v200, v100, vcc
	v_cmp_gt_u32_e32 vcc, 2.0, v17
	v_subrev_u32_e32 v17, 35, v16
	s_nop 0
	v_cndmask_b32_e32 v85, v200, v85, vcc
	v_cmp_gt_u32_e32 vcc, 2.0, v17
	v_add_u32_e32 v17, -8, v16
	s_nop 0
	v_cndmask_b32_e32 v101, v200, v101, vcc
	v_cmp_gt_u32_e32 vcc, 2.0, v17
	v_subrev_u32_e32 v17, 40, v16
	s_nop 0
	v_cndmask_b32_e32 v86, v200, v86, vcc
	v_cmp_gt_u32_e32 vcc, 2.0, v17
	v_add_u32_e32 v17, -9, v16
	s_nop 0
	v_cndmask_b32_e32 v102, v200, v102, vcc
	v_cmp_gt_u32_e32 vcc, 2.0, v17
	v_subrev_u32_e32 v17, 41, v16
	s_nop 0
	v_cndmask_b32_e32 v87, v200, v87, vcc
	v_cmp_gt_u32_e32 vcc, 2.0, v17
	v_add_u32_e32 v17, -10, v16
	s_nop 0
	v_cndmask_b32_e32 v103, v200, v103, vcc
	v_cmp_gt_u32_e32 vcc, 2.0, v17
	v_subrev_u32_e32 v17, 42, v16
	s_nop 0
	v_cndmask_b32_e32 v88, v200, v88, vcc
	v_cmp_gt_u32_e32 vcc, 2.0, v17
	v_add_u32_e32 v17, -11, v16
	s_nop 0
	v_cndmask_b32_e32 v104, v200, v104, vcc
	v_cmp_gt_u32_e32 vcc, 2.0, v17
	v_subrev_u32_e32 v17, 43, v16
	s_nop 0
	v_cndmask_b32_e32 v89, v200, v89, vcc
	v_cmp_gt_u32_e32 vcc, 2.0, v17
	v_add_u32_e32 v17, -16, v16
	s_nop 0
	v_cndmask_b32_e32 v105, v200, v105, vcc
	v_cmp_gt_u32_e32 vcc, 2.0, v17
	v_subrev_u32_e32 v17, 48, v16
	s_nop 0
	v_cndmask_b32_e32 v90, v200, v90, vcc
	v_cmp_gt_u32_e32 vcc, 2.0, v17
	v_subrev_u32_e32 v17, 17, v16
	s_nop 0
	v_cndmask_b32_e32 v106, v200, v106, vcc
	v_cmp_gt_u32_e32 vcc, 2.0, v17
	v_subrev_u32_e32 v17, 49, v16
	s_nop 0
	v_cndmask_b32_e32 v91, v200, v91, vcc
	v_cmp_gt_u32_e32 vcc, 2.0, v17
	v_subrev_u32_e32 v17, 18, v16
	s_nop 0
	v_cndmask_b32_e32 v107, v200, v107, vcc
	v_cmp_gt_u32_e32 vcc, 2.0, v17
	v_subrev_u32_e32 v17, 50, v16
	s_nop 0
	v_cndmask_b32_e32 v92, v200, v92, vcc
	v_cmp_gt_u32_e32 vcc, 2.0, v17
	v_subrev_u32_e32 v17, 19, v16
	s_nop 0
	v_cndmask_b32_e32 v108, v200, v108, vcc
	v_cmp_gt_u32_e32 vcc, 2.0, v17
	v_subrev_u32_e32 v17, 51, v16
	s_nop 0
	v_cndmask_b32_e32 v93, v200, v93, vcc
	v_cmp_gt_u32_e32 vcc, 2.0, v17
	v_subrev_u32_e32 v17, 24, v16
	s_nop 0
	v_cndmask_b32_e32 v109, v200, v109, vcc
	v_cmp_gt_u32_e32 vcc, 2.0, v17
	v_subrev_u32_e32 v17, 56, v16
	s_nop 0
	v_cndmask_b32_e32 v94, v200, v94, vcc
	v_cmp_gt_u32_e32 vcc, 2.0, v17
	v_subrev_u32_e32 v17, 25, v16
	s_nop 0
	v_cndmask_b32_e32 v110, v200, v110, vcc
	v_cmp_gt_u32_e32 vcc, 2.0, v17
	v_subrev_u32_e32 v17, 57, v16
	s_nop 0
	v_cndmask_b32_e32 v95, v200, v95, vcc
	v_cmp_gt_u32_e32 vcc, 2.0, v17
	v_subrev_u32_e32 v17, 26, v16
	s_nop 0
	v_cndmask_b32_e32 v111, v200, v111, vcc
	v_cmp_gt_u32_e32 vcc, 2.0, v17
	v_subrev_u32_e32 v17, 58, v16
	s_nop 0
	v_cndmask_b32_e32 v96, v200, v96, vcc
	v_cmp_gt_u32_e32 vcc, 2.0, v17
	v_subrev_u32_e32 v17, 27, v16
	v_subrev_u32_e32 v16, 59, v16
	v_cndmask_b32_e32 v112, v200, v112, vcc
	v_cmp_gt_u32_e32 vcc, 2.0, v17
	s_nop 1
	v_cndmask_b32_e32 v97, v200, v97, vcc
	v_cmp_gt_u32_e32 vcc, 2.0, v16
	s_nop 1
	v_cndmask_b32_e32 v113, v200, v113, vcc

; template <int MODE>
; __device__ __forceinline__ void partialSM(f32x16& p0, f32x16& p1, float& m_reg, float& mn, float& alpha) {
;     ...
;     constexpr float C2 = 1.4426950408889634f * SCALE;
;     if (__builtin_expect(__all((pmax - m_reg) * SCALE <= THR), 1)) { mn = m_reg; alpha = 1.f; }
;     else { mn = fmaxf(m_reg, pmax); alpha = __builtin_amdgcn_exp2f((m_reg - mn) * C2); m_reg = mn; }
;     const float mnL = -mn * C2;
; #pragma unroll
;     for (int r = 0; r < 16; ++r) p0[r] = fmaf(p0[r], C2, mnL);
; #pragma unroll
;     for (int r = 0; r < 16; ++r) p1[r] = fmaf(p1[r], C2, mnL);
; #pragma unroll
;     for (int r = 0; r < 16; ++r) p0[r] = __builtin_amdgcn_exp2f(p0[r]);
.LBB0_738:
	v_cndmask_b32_e64 v228, v5, v228, s[8:9]
	v_mul_f32_e32 v6, 0xbe0293ee, v228
	v_fmamk_f32 v5, v162, 0x3e0293ee, v6
	v_fmamk_f32 v7, v163, 0x3e0293ee, v6
	v_fmamk_f32 v8, v164, 0x3e0293ee, v6
	v_fmamk_f32 v9, v165, 0x3e0293ee, v6
	v_fmamk_f32 v10, v166, 0x3e0293ee, v6
	v_fmamk_f32 v11, v167, 0x3e0293ee, v6
	v_fmamk_f32 v12, v168, 0x3e0293ee, v6
	v_fmamk_f32 v13, v169, 0x3e0293ee, v6
	v_fmamk_f32 v14, v170, 0x3e0293ee, v6
	v_fmamk_f32 v15, v171, 0x3e0293ee, v6
	v_fmamk_f32 v20, v172, 0x3e0293ee, v6
	v_fmamk_f32 v21, v173, 0x3e0293ee, v6
	v_fmamk_f32 v22, v174, 0x3e0293ee, v6
	v_fmamk_f32 v23, v175, 0x3e0293ee, v6
	v_fmamk_f32 v24, v176, 0x3e0293ee, v6
	v_fmamk_f32 v25, v177, 0x3e0293ee, v6
	v_exp_f32_e32 v237, v5
	v_exp_f32_e32 v239, v7
	v_exp_f32_e32 v177, v8
	v_exp_f32_e32 v238, v9
	v_exp_f32_e32 v175, v10
	v_exp_f32_e32 v199, v11
	v_exp_f32_e32 v174, v12
	v_exp_f32_e32 v176, v13
	v_exp_f32_e32 v168, v14
	v_exp_f32_e32 v171, v15
	v_exp_f32_e32 v167, v20
	v_exp_f32_e32 v169, v21
	v_exp_f32_e32 v166, v22
	v_exp_f32_e32 v173, v23
	v_exp_f32_e32 v170, v24
	v_exp_f32_e32 v172, v25
	v_add_f32_e32 v2, v2, v16
	v_fmac_f32_e32 v2, v226, v227
	v_add_f32_e32 v227, v19, v32
	s_addk_i32 s37, 0x80
	s_add_i32 s36, s36, 2
	v_pk_fma_f32 v[160:161], v[160:161], s[24:25], v[6:7] op_sel_hi:[1,0,0]
	v_pk_fma_f32 v[158:159], v[158:159], s[24:25], v[6:7] op_sel_hi:[1,0,0]
	v_pk_fma_f32 v[156:157], v[156:157], s[24:25], v[6:7] op_sel_hi:[1,0,0]
	v_pk_fma_f32 v[154:155], v[154:155], s[24:25], v[6:7] op_sel_hi:[1,0,0]
	v_pk_fma_f32 v[152:153], v[152:153], s[24:25], v[6:7] op_sel_hi:[1,0,0]
	v_pk_fma_f32 v[150:151], v[150:151], s[24:25], v[6:7] op_sel_hi:[1,0,0]
	v_pk_fma_f32 v[162:163], v[148:149], s[24:25], v[6:7] op_sel_hi:[1,0,0]
	v_pk_fma_f32 v[164:165], v[146:147], s[24:25], v[6:7] op_sel_hi:[1,0,0]
	v_fmac_f32_e32 v227, v2, v17
	s_cmp_ge_i32 s36, s92
	v_add_u32_e32 v232, 0xffffff80, v232
	v_mov_b32_e32 v226, v4
	s_waitcnt lgkmcnt(0)
	s_barrier
	s_cbranch_scc1 .LBB0_781

; __device__ __forceinline__ void finishSM(f32x16& p0, f32x16& p1, float alpha, float& l_reg, bf16x8& pa0, bf16x8& pa1, bf16x8& pa2, bf16x8& pa3) {
;     ...
;     for (int r = 0; r < 16; ++r) p1[r] = __builtin_amdgcn_exp2f(p1[r]);
;     float ps = 0;
; #pragma unroll
;     for (int r = 0; r < 16; ++r) ps += p0[r];
; #pragma unroll
;     for (int r = 0; r < 16; ++r) ps += p1[r];
;     { auto rr = __builtin_amdgcn_permlane32_swap(__float_as_uint(ps), __float_as_uint(ps), false, false);
;       ps = __uint_as_float(rr[0]) + __uint_as_float(rr[1]); }
;     l_reg = l_reg * alpha + ps;
;     ...
;     PK4(p0, 0, pa0); PK4(p0, 8, pa1); PK4(p1, 0, pa2); PK4(p1, 8, pa3);
.LBB0_742:
	v_add_f32_e32 v2, v239, v237
	v_add_f32_e32 v2, v177, v2
	v_add_f32_e32 v2, v238, v2
	v_add_f32_e32 v2, v175, v2
	v_add_f32_e32 v2, v199, v2
	v_add_f32_e32 v2, v174, v2
	v_add_f32_e32 v2, v176, v2
	v_add_f32_e32 v2, v168, v2
	v_add_f32_e32 v2, v171, v2
	v_add_f32_e32 v2, v167, v2
	v_add_f32_e32 v2, v169, v2
	v_exp_f32_e32 v4, v164
	v_add_f32_e32 v2, v166, v2
	v_exp_f32_e32 v5, v165
	v_add_f32_e32 v2, v173, v2
	v_exp_f32_e32 v6, v162
	v_add_f32_e32 v2, v170, v2
	v_exp_f32_e32 v7, v163
	v_add_f32_e32 v2, v172, v2
	v_exp_f32_e32 v8, v150
	v_add_f32_e32 v2, v4, v2
	v_exp_f32_e32 v9, v151
	v_add_f32_e32 v2, v5, v2
	v_exp_f32_e32 v10, v152
	v_add_f32_e32 v2, v6, v2
	v_exp_f32_e32 v11, v153
	v_add_f32_e32 v2, v7, v2
	v_exp_f32_e32 v17, v154
	v_add_f32_e32 v2, v8, v2
	v_exp_f32_e32 v19, v155
	v_add_f32_e32 v2, v9, v2
	v_exp_f32_e32 v29, v156
	v_add_f32_e32 v2, v10, v2
	v_exp_f32_e32 v30, v157
	v_add_f32_e32 v2, v11, v2
	v_exp_f32_e32 v31, v158
	v_add_f32_e32 v2, v17, v2
	v_exp_f32_e32 v32, v159
	v_add_f32_e32 v2, v19, v2
	v_exp_f32_e32 v33, v160
	v_add_f32_e32 v2, v29, v2
	v_exp_f32_e32 v114, v161
	v_add_f32_e32 v2, v30, v2
	v_add_f32_e32 v2, v31, v2
	v_add_f32_e32 v2, v32, v2
	v_add_f32_e32 v2, v33, v2
	v_add_f32_e32 v2, v114, v2
	v_mov_b32_e32 v16, v2
	v_cvt_pk_bf16_f32 v12, v237, v239
	v_cvt_pk_bf16_f32 v13, v177, v238
	v_cvt_pk_bf16_f32 v14, v175, v199
	v_cvt_pk_bf16_f32 v15, v174, v176
	v_cvt_pk_bf16_f32 v20, v168, v171
	v_cvt_pk_bf16_f32 v21, v167, v169
	v_cvt_pk_bf16_f32 v22, v166, v173
	v_cvt_pk_bf16_f32 v23, v170, v172
	v_cvt_pk_bf16_f32 v24, v4, v5
	v_cvt_pk_bf16_f32 v25, v6, v7
	v_cvt_pk_bf16_f32 v26, v8, v9
	v_cvt_pk_bf16_f32 v27, v10, v11
	v_cvt_pk_bf16_f32 v28, v17, v19
	v_cvt_pk_bf16_f32 v29, v29, v30
	v_cvt_pk_bf16_f32 v30, v31, v32
	v_cvt_pk_bf16_f32 v31, v33, v114
	s_nop 1
	v_permlane32_swap_b32_e32 v2, v16
	v_permlane32_swap_b32_e32 v12, v14
	v_permlane32_swap_b32_e32 v13, v15
	v_permlane32_swap_b32_e32 v20, v22
	v_permlane32_swap_b32_e32 v21, v23
	v_permlane32_swap_b32_e32 v24, v26
	v_permlane32_swap_b32_e32 v25, v27
	v_permlane32_swap_b32_e32 v28, v30
	v_permlane32_swap_b32_e32 v29, v31
	s_add_i32 s63, s37, 0xffffffa0
	s_mul_hi_u32 s59, s63, s97
	s_mul_i32 s58, s63, s97
	s_sub_i32 s65, s37, 64
	v_lshl_add_u64 v[4:5], s[58:59], 1, v[200:201]
	s_mul_hi_u32 s59, s65, s97
	s_mul_i32 s58, s65, s97
	v_lshl_add_u64 v[8:9], s[58:59], 1, v[200:201]
	s_mul_hi_u32 s59, s63, s87
	s_mul_i32 s58, s63, s87
	v_lshl_add_u64 v[32:33], s[58:59], 1, v[202:203]
	s_add_i32 m0, s62, 0x8000
	s_mul_hi_u32 s59, s65, s87
	s_mul_i32 s58, s65, s87
	global_load_dwordx4 v[4:7], v[4:5], off
	s_nop 0
	global_load_dwordx4 v[8:11], v[8:9], off
	s_nop 0
	global_load_lds_dwordx4 v[32:33], off
	v_lshl_add_u64 v[32:33], s[58:59], 1, v[202:203]
	s_add_i32 m0, s62, 0xa000
	s_nop 0
	global_load_lds_dwordx4 v[32:33], off
	s_and_saveexec_b64 s[58:59], s[6:7]
	s_cbranch_execz .LBB0_744
	v_add_u32_e32 v17, s37, v213
	v_add_u32_e32 v17, 0xffffffa0, v17
	v_mad_u64_u32 v[32:33], vcc, v17, s96, 0
	v_ashrrev_i32_e32 v19, 31, v17
	v_mov_b32_e32 v114, v33
	v_mad_u64_u32 v[114:115], vcc, v19, s96, v[114:115]
	v_mov_b32_e32 v33, v114
	v_lshl_add_u64 v[32:33], v[32:33], 2, s[54:55]
	global_load_dword v207, v[32:33], off

; __device__ __forceinline__ void finishSM(f32x16& p0, f32x16& p1, float alpha, float& l_reg, bf16x8& pa0, bf16x8& pa1, bf16x8& pa2, bf16x8& pa3) {
;     ...
;     for (int r = 0; r < 16; ++r) p1[r] = __builtin_amdgcn_exp2f(p1[r]);
;     float ps = 0;
; #pragma unroll
;     for (int r = 0; r < 16; ++r) ps += p0[r];
; #pragma unroll
;     for (int r = 0; r < 16; ++r) ps += p1[r];
;     { auto rr = __builtin_amdgcn_permlane32_swap(__float_as_uint(ps), __float_as_uint(ps), false, false);
;       ps = __uint_as_float(rr[0]) + __uint_as_float(rr[1]); }
;     l_reg = l_reg * alpha + ps;
;     ...
;     PK4(p0, 0, pa0); PK4(p0, 8, pa1); PK4(p1, 0, pa2); PK4(p1, 8, pa3);
.LBB0_761:
	v_exp_f32_e32 v133, v134
	v_exp_f32_e32 v134, v135
	v_exp_f32_e32 v135, v136
	v_exp_f32_e32 v136, v137
	v_exp_f32_e32 v137, v138
	v_exp_f32_e32 v138, v139
	v_exp_f32_e32 v139, v140
	v_exp_f32_e32 v140, v141
	v_exp_f32_e32 v141, v142
	v_exp_f32_e32 v142, v143
	v_exp_f32_e32 v143, v144
	v_exp_f32_e32 v144, v145
	v_exp_f32_e32 v145, v12
	v_add_f32_e32 v12, v115, v114
	v_add_f32_e32 v12, v116, v12
	v_add_f32_e32 v12, v117, v12
	v_add_f32_e32 v12, v118, v12
	v_add_f32_e32 v12, v119, v12
	v_add_f32_e32 v12, v120, v12
	v_add_f32_e32 v12, v121, v12
	v_add_f32_e32 v12, v122, v12
	v_add_f32_e32 v12, v123, v12
	v_add_f32_e32 v12, v124, v12
	v_add_f32_e32 v12, v125, v12
	v_exp_f32_e32 v130, v13
	v_add_f32_e32 v12, v126, v12
	v_exp_f32_e32 v131, v14
	v_add_f32_e32 v12, v127, v12
	v_exp_f32_e32 v132, v15
	v_add_f32_e32 v12, v128, v12
	v_add_f32_e32 v12, v129, v12
	v_add_f32_e32 v12, v130, v12
	v_add_f32_e32 v12, v131, v12
	v_add_f32_e32 v12, v132, v12
	v_add_f32_e32 v12, v133, v12
	v_add_f32_e32 v12, v134, v12
	v_add_f32_e32 v12, v135, v12
	v_add_f32_e32 v12, v136, v12
	v_add_f32_e32 v12, v137, v12
	v_add_f32_e32 v12, v138, v12
	v_add_f32_e32 v12, v139, v12
	v_add_f32_e32 v12, v140, v12
	v_add_f32_e32 v12, v141, v12
	v_add_f32_e32 v12, v142, v12
	v_add_f32_e32 v12, v143, v12
	v_add_f32_e32 v12, v144, v12
	v_add_f32_e32 v19, v145, v12
	v_mov_b32_e32 v32, v19
	v_cvt_pk_bf16_f32 v12, v114, v115
	v_cvt_pk_bf16_f32 v13, v116, v117
	v_cvt_pk_bf16_f32 v14, v118, v119
	v_cvt_pk_bf16_f32 v15, v120, v121
	v_cvt_pk_bf16_f32 v20, v122, v123
	v_cvt_pk_bf16_f32 v21, v124, v125
	v_cvt_pk_bf16_f32 v22, v126, v127
	v_cvt_pk_bf16_f32 v23, v128, v129
	v_cvt_pk_bf16_f32 v24, v130, v131
	v_cvt_pk_bf16_f32 v25, v132, v133
	v_cvt_pk_bf16_f32 v26, v134, v135
	v_cvt_pk_bf16_f32 v27, v136, v137
	v_cvt_pk_bf16_f32 v28, v138, v139
	v_cvt_pk_bf16_f32 v29, v140, v141
	v_cvt_pk_bf16_f32 v30, v142, v143
	v_cvt_pk_bf16_f32 v31, v144, v145
	s_nop 1
	v_permlane32_swap_b32_e32 v19, v32
	v_permlane32_swap_b32_e32 v12, v14
	v_permlane32_swap_b32_e32 v13, v15
	v_permlane32_swap_b32_e32 v20, v22
	v_permlane32_swap_b32_e32 v21, v23
	v_permlane32_swap_b32_e32 v24, v26
	v_permlane32_swap_b32_e32 v25, v27
	v_permlane32_swap_b32_e32 v28, v30
	v_permlane32_swap_b32_e32 v29, v31
	s_add_i32 s60, s36, 1
	s_cmp_lt_i32 s60, s92
	s_cselect_b64 s[10:11], -1, 0
	s_cmp_ge_i32 s60, s92
	s_cbranch_scc0 .LBB0_764
	s_and_b64 vcc, exec, s[8:9]
	s_cbranch_vccz .LBB0_767

; #define SBAR() __builtin_amdgcn_sched_barrier(0)
; #define ACT(t) (KBASE(t) <= qlo + QBLK - 1 && KBASE(t) + KVBLK - 1 >= qlo - W + 1)
; #define ACT(t) (KBASE(t) <= qlo + QBLK - 1 && KBASE(t) + KVBLK - 1 >= qlo - W + 1)
; #define ACT(t) (KBASE(t) <= qlo + QBLK - 1 && KBASE(t) + KVBLK - 1 >= qlo - W + 1)
; __device__ __forceinline__ void finishSM(f32x16& p0, f32x16& p1, float alpha, float& l_reg, bf16x8& pa0, bf16x8& pa1, bf16x8& pa2, bf16x8& pa3) {
;     ...
;     for (int r = 0; r < 16; ++r) p1[r] = __builtin_amdgcn_exp2f(p1[r]);
;     float ps = 0;
; #pragma unroll
;     for (int r = 0; r < 16; ++r) ps += p0[r];
; #pragma unroll
;     for (int r = 0; r < 16; ++r) ps += p1[r];
;     { auto rr = __builtin_amdgcn_permlane32_swap(__float_as_uint(ps), __float_as_uint(ps), false, false);
;       ps = __uint_as_float(rr[0]) + __uint_as_float(rr[1]); }
;     l_reg = l_reg * alpha + ps;
;     ...
;     PK4(p0, 0, pa0); PK4(p0, 8, pa1); PK4(p1, 0, pa2); PK4(p1, 8, pa3);
; template <int MODE>
; __device__ __forceinline__ void attn_block_pipe(const BlockRef& cur, const BlockRef& nxt, char* lds, LAS unsigned char* ldsl, Seam<MODE>& S) {
;     ...
;     QLOAD(nxt);
;     SBAR();
;     finishSM(pA0, pA1, alA, l_reg, pa0, pa1, pa2, pa3); SBAR();
;     PPV<0, SK>(o, vb0, pa0, pa1, pa2, pa3, ACT(even ? NT - 2 : NT - 1));
.LBB0_788:
	s_or_b64 exec, exec, s[8:9]
	s_add_i32 s8, s93, s83
	s_ashr_i32 s9, s8, 31
	s_mul_i32 s9, s9, s81
	s_mul_hi_u32 s10, s8, s81
	s_add_i32 s9, s10, s9
	s_mul_i32 s8, s8, s81
	v_mul_lo_u32 v1, s81, v214
	s_lshl_b64 s[8:9], s[8:9], 1
	v_lshlrev_b32_e32 v1, 1, v1
	s_add_u32 s8, s70, s8
	v_lshl_or_b32 v1, v220, 4, v1
	s_addc_u32 s9, s71, s9
	global_load_dwordx4 v[190:193], v1, s[8:9]
	global_load_dwordx4 v[186:189], v1, s[8:9] offset:32
	global_load_dwordx4 v[182:185], v1, s[8:9] offset:64
	global_load_dwordx4 v[178:181], v1, s[8:9] offset:96
	global_load_dwordx4 v[12:15], v1, s[8:9] offset:128
	global_load_dwordx4 v[20:23], v1, s[8:9] offset:160
	global_load_dwordx4 v[24:27], v1, s[8:9] offset:192
	global_load_dwordx4 v[28:31], v1, s[8:9] offset:224
	v_add_f32_e32 v1, v239, v237
	v_add_f32_e32 v1, v177, v1
	v_add_f32_e32 v1, v238, v1
	v_add_f32_e32 v1, v175, v1
	v_add_f32_e32 v1, v199, v1
	v_add_f32_e32 v1, v174, v1
	v_add_f32_e32 v1, v176, v1
	v_add_f32_e32 v1, v168, v1
	v_add_f32_e32 v1, v171, v1
	v_add_f32_e32 v1, v167, v1
	v_add_f32_e32 v1, v169, v1
	v_exp_f32_e32 v16, v164
	v_add_f32_e32 v1, v166, v1
	v_exp_f32_e32 v17, v165
	v_add_f32_e32 v1, v173, v1
	v_exp_f32_e32 v19, v162
	v_add_f32_e32 v1, v170, v1
	v_exp_f32_e32 v32, v163
	v_add_f32_e32 v1, v172, v1
	v_exp_f32_e32 v33, v150
	v_add_f32_e32 v1, v16, v1
	v_exp_f32_e32 v99, v151
	v_add_f32_e32 v1, v17, v1
	v_exp_f32_e32 v111, v152
	v_add_f32_e32 v1, v19, v1
	v_exp_f32_e32 v112, v153
	v_add_f32_e32 v1, v32, v1
	v_exp_f32_e32 v146, v154
	v_add_f32_e32 v1, v33, v1
	v_exp_f32_e32 v147, v155
	v_add_f32_e32 v1, v99, v1
	v_exp_f32_e32 v148, v156
	v_add_f32_e32 v1, v111, v1
	v_exp_f32_e32 v149, v157
	v_add_f32_e32 v1, v112, v1
	v_exp_f32_e32 v150, v158
	v_add_f32_e32 v1, v146, v1
	v_exp_f32_e32 v151, v159
	v_add_f32_e32 v1, v147, v1
	v_exp_f32_e32 v152, v160
	v_add_f32_e32 v1, v148, v1
	v_exp_f32_e32 v153, v161
	v_add_f32_e32 v1, v149, v1
	v_add_f32_e32 v1, v150, v1
	v_add_f32_e32 v1, v151, v1
	v_add_f32_e32 v1, v152, v1
	v_add_f32_e32 v1, v153, v1
	v_mov_b32_e32 v2, v1
	v_cvt_pk_bf16_f32 v100, v237, v239
	v_cvt_pk_bf16_f32 v101, v177, v238
	v_cvt_pk_bf16_f32 v102, v175, v199
	v_cvt_pk_bf16_f32 v103, v174, v176
	v_cvt_pk_bf16_f32 v104, v168, v171
	v_cvt_pk_bf16_f32 v105, v167, v169
	v_cvt_pk_bf16_f32 v106, v166, v173
	v_cvt_pk_bf16_f32 v107, v170, v172
	v_cvt_pk_bf16_f32 v108, v16, v17
	v_cvt_pk_bf16_f32 v109, v19, v32
	v_cvt_pk_bf16_f32 v110, v33, v99
	v_cvt_pk_bf16_f32 v111, v111, v112
	v_cvt_pk_bf16_f32 v146, v146, v147
	v_cvt_pk_bf16_f32 v147, v148, v149
	v_cvt_pk_bf16_f32 v148, v150, v151
	v_cvt_pk_bf16_f32 v149, v152, v153
	s_nop 1
	v_permlane32_swap_b32_e32 v1, v2
	v_permlane32_swap_b32_e32 v100, v102
	v_permlane32_swap_b32_e32 v101, v103
	v_permlane32_swap_b32_e32 v104, v106
	v_permlane32_swap_b32_e32 v105, v107
	v_permlane32_swap_b32_e32 v108, v110
	v_permlane32_swap_b32_e32 v109, v111
	v_permlane32_swap_b32_e32 v146, v148
	v_permlane32_swap_b32_e32 v147, v149
	s_or_b32 s8, s92, -2
	s_add_i32 s8, s8, s90
	s_lshl_b32 s10, s8, 6
	s_cmp_le_i32 s10, s91
	s_cselect_b64 s[8:9], -1, 0
	s_or_b32 s10, s10, 63
	s_cmp_gt_i32 s10, s95
	s_cselect_b64 s[10:11], -1, 0
	s_and_b64 s[8:9], s[8:9], s[10:11]
	s_andn2_b64 vcc, exec, s[8:9]
	s_cbranch_vccnz .LBB0_790
	ds_read_b64_tr_b16 v[150:151], v219 offset:0
	ds_read_b64_tr_b16 v[152:153], v219 offset:0x800
	ds_read_b64_tr_b16 v[154:155], v219 offset:0x1000
	ds_read_b64_tr_b16 v[156:157], v219 offset:0x1800
	ds_read_b64_tr_b16 v[158:159], v219 offset:0x2000
	ds_read_b64_tr_b16 v[160:161], v219 offset:0x2800
	ds_read_b64_tr_b16 v[162:163], v219 offset:0x3000
	ds_read_b64_tr_b16 v[164:165], v219 offset:0x3800
	s_waitcnt lgkmcnt(0)
	s_nop 0
	v_mfma_f32_32x32x16_bf16 v[82:97], v[100:103], v[150:153], v[82:97]
	ds_read_b64_tr_b16 v[150:151], v219 offset:0x200
	ds_read_b64_tr_b16 v[152:153], v219 offset:0xa00
	v_mfma_f32_32x32x16_bf16 v[82:97], v[104:107], v[154:157], v[82:97]
	ds_read_b64_tr_b16 v[154:155], v219 offset:0x1200
	ds_read_b64_tr_b16 v[156:157], v219 offset:0x1a00
	v_mfma_f32_32x32x16_bf16 v[82:97], v[108:111], v[158:161], v[82:97]
	ds_read_b64_tr_b16 v[158:159], v219 offset:0x2200
	ds_read_b64_tr_b16 v[160:161], v219 offset:0x2a00
	ds_read_b64_tr_b16 v[166:167], v219 offset:0x3200
	ds_read_b64_tr_b16 v[168:169], v219 offset:0x3a00
	s_waitcnt lgkmcnt(0)
	v_mfma_f32_32x32x16_bf16 v[82:97], v[146:149], v[162:165], v[82:97]
	v_mfma_f32_32x32x16_bf16 v[66:81], v[100:103], v[150:153], v[66:81]
	ds_read_b64_tr_b16 v[150:151], v219 offset:0x400
	ds_read_b64_tr_b16 v[152:153], v219 offset:0xc00
	v_mfma_f32_32x32x16_bf16 v[66:81], v[104:107], v[154:157], v[66:81]
	ds_read_b64_tr_b16 v[154:155], v219 offset:0x1400
	ds_read_b64_tr_b16 v[156:157], v219 offset:0x1c00
	v_mfma_f32_32x32x16_bf16 v[66:81], v[108:111], v[158:161], v[66:81]
	ds_read_b64_tr_b16 v[158:159], v219 offset:0x2400
	ds_read_b64_tr_b16 v[160:161], v219 offset:0x2c00
	ds_read_b64_tr_b16 v[162:163], v219 offset:0x3400
	ds_read_b64_tr_b16 v[164:165], v219 offset:0x3c00
	s_waitcnt lgkmcnt(0)
	v_mfma_f32_32x32x16_bf16 v[66:81], v[146:149], v[166:169], v[66:81]
	v_mfma_f32_32x32x16_bf16 v[50:65], v[100:103], v[150:153], v[50:65]
	ds_read_b64_tr_b16 v[150:151], v219 offset:0x600
	ds_read_b64_tr_b16 v[152:153], v219 offset:0xe00
	v_mfma_f32_32x32x16_bf16 v[50:65], v[104:107], v[154:157], v[50:65]
	ds_read_b64_tr_b16 v[154:155], v219 offset:0x1600
	ds_read_b64_tr_b16 v[156:157], v219 offset:0x1e00
	v_mfma_f32_32x32x16_bf16 v[50:65], v[108:111], v[158:161], v[50:65]
	ds_read_b64_tr_b16 v[158:159], v219 offset:0x2600
	ds_read_b64_tr_b16 v[160:161], v219 offset:0x2e00
	ds_read_b64_tr_b16 v[166:167], v219 offset:0x3600
	ds_read_b64_tr_b16 v[168:169], v219 offset:0x3e00
	s_waitcnt lgkmcnt(0)
	v_mfma_f32_32x32x16_bf16 v[50:65], v[146:149], v[162:165], v[50:65]
	v_mfma_f32_32x32x16_bf16 v[34:49], v[100:103], v[150:153], v[34:49]
	v_mfma_f32_32x32x16_bf16 v[34:49], v[104:107], v[154:157], v[34:49]
	v_mfma_f32_32x32x16_bf16 v[34:49], v[108:111], v[158:161], v[34:49]
	v_mfma_f32_32x32x16_bf16 v[34:49], v[146:149], v[166:169], v[34:49]

; template <int MODE>
; __device__ __forceinline__ void partialSM(f32x16& p0, f32x16& p1, float& m_reg, float& mn, float& alpha) {
;     ...
;     else { mn = fmaxf(m_reg, pmax); alpha = __builtin_amdgcn_exp2f((m_reg - mn) * C2); m_reg = mn; }
;     const float mnL = -mn * C2;
; #pragma unroll
;     for (int r = 0; r < 16; ++r) p0[r] = fmaf(p0[r], C2, mnL);
; #pragma unroll
;     for (int r = 0; r < 16; ++r) p1[r] = fmaf(p1[r], C2, mnL);
; #pragma unroll
;     for (int r = 0; r < 16; ++r) p0[r] = __builtin_amdgcn_exp2f(p0[r]);
; }
; __device__ __forceinline__ void finishSM(f32x16& p0, f32x16& p1, float alpha, float& l_reg, bf16x8& pa0, bf16x8& pa1, bf16x8& pa2, bf16x8& pa3) {
; #pragma unroll
;     for (int r = 0; r < 16; ++r) p1[r] = __builtin_amdgcn_exp2f(p1[r]);
;     float ps = 0;
; #pragma unroll
;     for (int r = 0; r < 16; ++r) ps += p0[r];
; #pragma unroll
;     for (int r = 0; r < 16; ++r) ps += p1[r];
;     { auto rr = __builtin_amdgcn_permlane32_swap(__float_as_uint(ps), __float_as_uint(ps), false, false);
;       ps = __uint_as_float(rr[0]) + __uint_as_float(rr[1]); }
;     l_reg = l_reg * alpha + ps;
.LBB0_801:
	v_cndmask_b32_e64 v228, v16, v228, s[6:7]
	v_mul_f32_e32 v16, 0xbe0293ee, v228
	v_fmamk_f32 v19, v114, 0x3e0293ee, v16
	v_fmamk_f32 v32, v115, 0x3e0293ee, v16
	v_exp_f32_e32 v98, v19
	v_fmamk_f32 v33, v116, 0x3e0293ee, v16
	v_exp_f32_e32 v110, v32
	v_fmamk_f32 v100, v117, 0x3e0293ee, v16
	v_fmamk_f32 v101, v118, 0x3e0293ee, v16
	v_fmamk_f32 v102, v119, 0x3e0293ee, v16
	v_fmamk_f32 v103, v120, 0x3e0293ee, v16
	v_fmamk_f32 v105, v122, 0x3e0293ee, v16
	v_fmamk_f32 v106, v123, 0x3e0293ee, v16
	v_fmamk_f32 v123, v124, 0x3e0293ee, v16
	v_fmamk_f32 v124, v125, 0x3e0293ee, v16
	v_exp_f32_e32 v99, v33
	v_fmamk_f32 v104, v121, 0x3e0293ee, v16
	v_fmamk_f32 v125, v126, 0x3e0293ee, v16
	v_fmamk_f32 v126, v127, 0x3e0293ee, v16
	v_fmamk_f32 v127, v128, 0x3e0293ee, v16
	v_fmamk_f32 v128, v129, 0x3e0293ee, v16
	v_fmamk_f32 v17, v130, 0x3e0293ee, v16
	v_fmamk_f32 v111, v131, 0x3e0293ee, v16
	v_fmamk_f32 v112, v132, 0x3e0293ee, v16
	v_fmamk_f32 v113, v133, 0x3e0293ee, v16
	v_fmamk_f32 v114, v134, 0x3e0293ee, v16
	v_fmamk_f32 v115, v135, 0x3e0293ee, v16
	v_fmamk_f32 v116, v136, 0x3e0293ee, v16
	v_fmamk_f32 v117, v137, 0x3e0293ee, v16
	v_fmamk_f32 v118, v138, 0x3e0293ee, v16
	v_fmamk_f32 v119, v139, 0x3e0293ee, v16
	v_fmamk_f32 v120, v140, 0x3e0293ee, v16
	v_fmamk_f32 v121, v141, 0x3e0293ee, v16
	v_fmamk_f32 v122, v142, 0x3e0293ee, v16
	v_exp_f32_e32 v109, v100
	v_exp_f32_e32 v100, v101
	v_exp_f32_e32 v108, v102
	v_exp_f32_e32 v101, v103
	v_exp_f32_e32 v102, v105
	v_exp_f32_e32 v103, v123
	v_exp_f32_e32 v105, v124
	v_fmamk_f32 v123, v143, 0x3e0293ee, v16
	v_fmamk_f32 v124, v144, 0x3e0293ee, v16
	v_fmac_f32_e32 v16, 0x3e0293ee, v145
	v_exp_f32_e32 v107, v104
	v_exp_f32_e32 v104, v126
	v_exp_f32_e32 v126, v16
	v_add_f32_e32 v16, v110, v98
	v_add_f32_e32 v16, v99, v16
	v_add_f32_e32 v16, v109, v16
	v_add_f32_e32 v16, v100, v16
	v_exp_f32_e32 v106, v106
	v_add_f32_e32 v16, v108, v16
	v_add_f32_e32 v16, v101, v16
	v_add_f32_e32 v16, v107, v16
	v_exp_f32_e32 v32, v125
	v_add_f32_e32 v16, v102, v16
	v_add_f32_e32 v16, v106, v16
	v_exp_f32_e32 v19, v127
	v_add_f32_e32 v16, v103, v16
	v_exp_f32_e32 v33, v128
	v_add_f32_e32 v16, v105, v16
	v_exp_f32_e32 v125, v17
	v_add_f32_e32 v16, v32, v16
	v_exp_f32_e32 v111, v111
	v_add_f32_e32 v16, v104, v16
	v_exp_f32_e32 v112, v112
	v_add_f32_e32 v16, v19, v16
	v_exp_f32_e32 v113, v113
	v_add_f32_e32 v16, v33, v16
	v_exp_f32_e32 v114, v114
	v_add_f32_e32 v16, v125, v16
	v_exp_f32_e32 v115, v115
	v_add_f32_e32 v16, v111, v16
	v_exp_f32_e32 v116, v116
	v_add_f32_e32 v16, v112, v16
	v_exp_f32_e32 v117, v117
	v_add_f32_e32 v16, v113, v16
	v_exp_f32_e32 v118, v118
	v_add_f32_e32 v16, v114, v16
	v_exp_f32_e32 v119, v119
	v_add_f32_e32 v16, v115, v16
	v_exp_f32_e32 v120, v120
	v_add_f32_e32 v16, v116, v16
	v_exp_f32_e32 v121, v121
	v_add_f32_e32 v16, v117, v16
	v_exp_f32_e32 v122, v122
	v_add_f32_e32 v16, v118, v16
	v_exp_f32_e32 v123, v123
	v_add_f32_e32 v16, v119, v16
	v_exp_f32_e32 v124, v124
	v_add_f32_e32 v16, v120, v16
	v_add_f32_e32 v16, v121, v16
	v_add_f32_e32 v16, v122, v16
	v_add_f32_e32 v16, v123, v16
	v_add_f32_e32 v16, v124, v16
	v_add_f32_e32 v16, v126, v16
	v_mov_b32_e32 v17, v16
	v_cvt_pk_bf16_f32 v98, v98, v110
	v_cvt_pk_bf16_f32 v99, v99, v109
	v_cvt_pk_bf16_f32 v100, v100, v108
	v_cvt_pk_bf16_f32 v101, v101, v107
	v_cvt_pk_bf16_f32 v102, v102, v106
	v_cvt_pk_bf16_f32 v103, v103, v105
	v_cvt_pk_bf16_f32 v104, v32, v104
	v_cvt_pk_bf16_f32 v105, v19, v33
	v_cvt_pk_bf16_f32 v106, v125, v111
	v_cvt_pk_bf16_f32 v107, v112, v113
	v_cvt_pk_bf16_f32 v108, v114, v115
	v_cvt_pk_bf16_f32 v109, v116, v117
	v_cvt_pk_bf16_f32 v110, v118, v119
	v_cvt_pk_bf16_f32 v111, v120, v121
	v_cvt_pk_bf16_f32 v112, v122, v123
	v_cvt_pk_bf16_f32 v113, v124, v126
	s_nop 1
	v_permlane32_swap_b32_e32 v16, v17
	v_permlane32_swap_b32_e32 v98, v100
	v_permlane32_swap_b32_e32 v99, v101
	v_permlane32_swap_b32_e32 v102, v104
	v_permlane32_swap_b32_e32 v103, v105
	v_permlane32_swap_b32_e32 v106, v108
	v_permlane32_swap_b32_e32 v107, v109
	v_permlane32_swap_b32_e32 v110, v112
	v_permlane32_swap_b32_e32 v111, v113
	s_add_i32 s6, s89, 0xffffff80
	s_cmp_gt_i32 s19, s6
	s_cselect_b64 s[6:7], -1, 0
	s_and_b64 s[6:7], s[8:9], s[6:7]
	s_andn2_b64 vcc, exec, s[6:7]
	s_cbranch_vccnz .LBB0_803
; template <int VB, bool SK>
; __device__ __forceinline__ void pv_tile(f32x16* o, int vb0, bf16x8 pa0, bf16x8 pa1, bf16x8 pa2, bf16x8 pa3, bool act) {
;     if (SK && !act) return;
;     ...
;     if (ATT_PRIO) __builtin_amdgcn_s_setprio(1);
;     PV_D0(0); PV_D0(1); PV_D0(2); PV_D0(3);
	ds_read_b64_tr_b16 v[114:115], v219 offset:0x4000
	ds_read_b64_tr_b16 v[116:117], v219 offset:0x4800
	ds_read_b64_tr_b16 v[118:119], v219 offset:0x5000
	ds_read_b64_tr_b16 v[120:121], v219 offset:0x5800
	ds_read_b64_tr_b16 v[122:123], v219 offset:0x6000
	ds_read_b64_tr_b16 v[124:125], v219 offset:0x6800
	ds_read_b64_tr_b16 v[126:127], v219 offset:0x7000
	ds_read_b64_tr_b16 v[128:129], v219 offset:0x7800
	s_waitcnt lgkmcnt(0)
	s_nop 0
	v_mfma_f32_32x32x16_bf16 v[82:97], v[98:101], v[114:117], v[82:97]
	ds_read_b64_tr_b16 v[114:115], v219 offset:0x4200
	ds_read_b64_tr_b16 v[116:117], v219 offset:0x4a00
	v_mfma_f32_32x32x16_bf16 v[82:97], v[102:105], v[118:121], v[82:97]
	ds_read_b64_tr_b16 v[118:119], v219 offset:0x5200
	ds_read_b64_tr_b16 v[120:121], v219 offset:0x5a00
	v_mfma_f32_32x32x16_bf16 v[82:97], v[106:109], v[122:125], v[82:97]
	ds_read_b64_tr_b16 v[122:123], v219 offset:0x6200
	ds_read_b64_tr_b16 v[124:125], v219 offset:0x6a00
	ds_read_b64_tr_b16 v[130:131], v219 offset:0x7200
	ds_read_b64_tr_b16 v[132:133], v219 offset:0x7a00
	s_waitcnt lgkmcnt(0)
	v_mfma_f32_32x32x16_bf16 v[82:97], v[110:113], v[126:129], v[82:97]
	v_mfma_f32_32x32x16_bf16 v[66:81], v[98:101], v[114:117], v[66:81]
	ds_read_b64_tr_b16 v[114:115], v219 offset:0x4400
	ds_read_b64_tr_b16 v[116:117], v219 offset:0x4c00
	v_mfma_f32_32x32x16_bf16 v[66:81], v[102:105], v[118:121], v[66:81]
	ds_read_b64_tr_b16 v[118:119], v219 offset:0x5400
	ds_read_b64_tr_b16 v[120:121], v219 offset:0x5c00
	v_mfma_f32_32x32x16_bf16 v[66:81], v[106:109], v[122:125], v[66:81]
	ds_read_b64_tr_b16 v[122:123], v219 offset:0x6400
	ds_read_b64_tr_b16 v[124:125], v219 offset:0x6c00
	ds_read_b64_tr_b16 v[126:127], v219 offset:0x7400
	ds_read_b64_tr_b16 v[128:129], v219 offset:0x7c00
	s_waitcnt lgkmcnt(0)
	v_mfma_f32_32x32x16_bf16 v[66:81], v[110:113], v[130:133], v[66:81]
	v_mfma_f32_32x32x16_bf16 v[50:65], v[98:101], v[114:117], v[50:65]
	ds_read_b64_tr_b16 v[114:115], v219 offset:0x4600
	ds_read_b64_tr_b16 v[116:117], v219 offset:0x4e00
	v_mfma_f32_32x32x16_bf16 v[50:65], v[102:105], v[118:121], v[50:65]
	ds_read_b64_tr_b16 v[118:119], v219 offset:0x5600
	ds_read_b64_tr_b16 v[120:121], v219 offset:0x5e00
	v_mfma_f32_32x32x16_bf16 v[50:65], v[106:109], v[122:125], v[50:65]
	ds_read_b64_tr_b16 v[122:123], v219 offset:0x6600
	ds_read_b64_tr_b16 v[124:125], v219 offset:0x6e00
	ds_read_b64_tr_b16 v[130:131], v219 offset:0x7600
	ds_read_b64_tr_b16 v[132:133], v219 offset:0x7e00
	s_waitcnt lgkmcnt(0)
	v_mfma_f32_32x32x16_bf16 v[50:65], v[110:113], v[126:129], v[50:65]
	v_mfma_f32_32x32x16_bf16 v[34:49], v[98:101], v[114:117], v[34:49]
	v_mfma_f32_32x32x16_bf16 v[34:49], v[102:105], v[118:121], v[34:49]
	v_mfma_f32_32x32x16_bf16 v[34:49], v[106:109], v[122:125], v[34:49]
	v_mfma_f32_32x32x16_bf16 v[34:49], v[110:113], v[130:133], v[34:49]

; template <int MODE>
; __device__ __forceinline__ void partialSM(f32x16& p0, f32x16& p1, float& m_reg, float& mn, float& alpha) {
;     ...
;     if (__builtin_expect(__all((pmax - m_reg) * SCALE <= THR), 1)) { mn = m_reg; alpha = 1.f; }
;     else { mn = fmaxf(m_reg, pmax); alpha = __builtin_amdgcn_exp2f((m_reg - mn) * C2); m_reg = mn; }
;     const float mnL = -mn * C2;
; #pragma unroll
;     for (int r = 0; r < 16; ++r) p0[r] = fmaf(p0[r], C2, mnL);
; #pragma unroll
;     for (int r = 0; r < 16; ++r) p1[r] = fmaf(p1[r], C2, mnL);
; #pragma unroll
;     for (int r = 0; r < 16; ++r) p0[r] = __builtin_amdgcn_exp2f(p0[r]);
; }
; template <int KB, bool SK, bool ROPE, bool QHALF>
; __device__ __forceinline__ void qkt(f32x16& p0, f32x16& p1, const char* lds, int r32, int hi, const bf16x8* qr, const char* qrl, bool act) {
;     if (SK && !act) { const float NEG = -__builtin_inff();
; #pragma unroll
;         for (int r = 0; r < 16; ++r) { p0[r] = NEG; p1[r] = NEG; } return; }
;     p0 = f32x16{}; p1 = f32x16{};
;     ...
;     if (ATT_PRIO) __builtin_amdgcn_s_setprio(1);
;     const char* kb[4];
; #pragma unroll
;     for (int dd = 0; dd < 4; ++dd) kb[dd] = lds + OFF_K + KB * SHM_K + KSWZ(r32, (dd * 16 + hi * 8) * 2);
; #pragma unroll
;     for (int d0 = 0; d0 < 8; ++d0) { const char* a = kb[d0 & 3] + (d0 >> 2) * 128;
;         bf16x8 b0 = *reinterpret_cast<const bf16x8*>(a);
;         bf16x8 b1 = *reinterpret_cast<const bf16x8*>(a + 32 * 256);
;         bf16x8 qf;
;         if constexpr (QHALF) { if (d0 >= 4) qf = *reinterpret_cast<const bf16x8*>(qrl + (d0 - 4) * 1024); else qf = qr[d0]; } else qf = qr[d0];
;         p0 = __builtin_amdgcn_mfma_f32_32x32x16_bf16(b0, qf, p0, 0, 0, 0);
;         p1 = __builtin_amdgcn_mfma_f32_32x32x16_bf16(b1, qf, p1, 0, 0, 0); }
;     if constexpr (ROPE) {
; #pragma unroll
;         for (int d0 = 0; d0 < 4; ++d0) { const char* a = lds + OFF_KR + KB * SHM_KR + KRSWZ(r32, 2 * d0 + hi);
;             bf16x8 b0 = *reinterpret_cast<const bf16x8*>(a);
;             bf16x8 b1 = *reinterpret_cast<const bf16x8*>(a + 32 * 128);
;             const bf16x8 qf = *reinterpret_cast<const bf16x8*>(qrl + d0 * 1024);
;             p0 = __builtin_amdgcn_mfma_f32_32x32x16_bf16(b0, qf, p0, 0, 0, 0);
;             p1 = __builtin_amdgcn_mfma_f32_32x32x16_bf16(b1, qf, p1, 0, 0, 0); }
;     }
.LBB0_1035:
	v_cndmask_b32_e64 v178, v5, v227, s[6:7]
	v_mul_f32_e32 v6, 0xbdd53b94, v178
	v_fmamk_f32 v13, v137, 0x3dd53b94, v6
	v_fmamk_f32 v137, v141, 0x3dd53b94, v6
	v_fmamk_f32 v5, v130, 0x3dd53b94, v6
	v_fmamk_f32 v7, v131, 0x3dd53b94, v6
	v_fmamk_f32 v8, v132, 0x3dd53b94, v6
	v_fmamk_f32 v9, v133, 0x3dd53b94, v6
	v_fmamk_f32 v10, v134, 0x3dd53b94, v6
	v_fmamk_f32 v11, v135, 0x3dd53b94, v6
	v_fmamk_f32 v12, v136, 0x3dd53b94, v6
	v_fmamk_f32 v14, v138, 0x3dd53b94, v6
	v_fmamk_f32 v15, v139, 0x3dd53b94, v6
	v_fmamk_f32 v136, v140, 0x3dd53b94, v6
	v_fmamk_f32 v138, v142, 0x3dd53b94, v6
	v_fmamk_f32 v139, v143, 0x3dd53b94, v6
	v_fmamk_f32 v140, v144, 0x3dd53b94, v6
	v_fmamk_f32 v141, v145, 0x3dd53b94, v6
	v_exp_f32_e32 v188, v5
	v_exp_f32_e32 v227, v7
	v_exp_f32_e32 v186, v8
	v_exp_f32_e32 v189, v9
	v_exp_f32_e32 v185, v10
	v_exp_f32_e32 v187, v11
	v_exp_f32_e32 v183, v12
	v_exp_f32_e32 v184, v13
	v_exp_f32_e32 v179, v14
	v_exp_f32_e32 v182, v15
	v_exp_f32_e32 v144, v136
	v_exp_f32_e32 v180, v137
	v_exp_f32_e32 v142, v138
	v_exp_f32_e32 v181, v139
	v_exp_f32_e32 v143, v140
	v_exp_f32_e32 v145, v141
	v_add_f32_e32 v5, v195, v225
	v_fmac_f32_e32 v5, v220, v191
	v_add_f32_e32 v191, v228, v229
	s_addk_i32 s42, 0x80
	s_add_i32 s36, s36, 2
	v_pk_fma_f32 v[128:129], v[128:129], s[14:15], v[6:7] op_sel_hi:[1,0,0]
	v_pk_fma_f32 v[126:127], v[126:127], s[14:15], v[6:7] op_sel_hi:[1,0,0]
	v_pk_fma_f32 v[130:131], v[124:125], s[14:15], v[6:7] op_sel_hi:[1,0,0]
	v_pk_fma_f32 v[132:133], v[122:123], s[14:15], v[6:7] op_sel_hi:[1,0,0]
	v_pk_fma_f32 v[134:135], v[120:121], s[14:15], v[6:7] op_sel_hi:[1,0,0]
	v_pk_fma_f32 v[136:137], v[118:119], s[14:15], v[6:7] op_sel_hi:[1,0,0]
	v_pk_fma_f32 v[138:139], v[116:117], s[14:15], v[6:7] op_sel_hi:[1,0,0]
	v_pk_fma_f32 v[140:141], v[114:115], s[14:15], v[6:7] op_sel_hi:[1,0,0]
	v_fmac_f32_e32 v191, v5, v226
	s_cmp_ge_i32 s36, s63
	v_add_u32_e32 v193, 0xffffff80, v193
	v_mov_b32_e32 v220, v4
	s_waitcnt lgkmcnt(0)
	s_cbranch_scc0 .Lmy_nobar_1
	s_barrier
	s_branch .LBB0_1052
.Lmy_nobar_1:
.LBB0_1036:
	ds_read_b128 v[4:7], v212 offset:49152
	ds_read_b128 v[8:11], v212 offset:57344
	s_add_i32 s10, 0, 0x12800
	v_exp_f32_e32 v122, v132
	v_exp_f32_e32 v123, v133
	s_waitcnt lgkmcnt(1)
	v_mfma_f32_32x32x16_bf16 v[102:117], v[4:7], v[174:177], 0
	v_exp_f32_e32 v124, v130
	v_exp_f32_e32 v125, v131
	v_exp_f32_e32 v126, v126
	v_exp_f32_e32 v127, v127
	v_exp_f32_e32 v128, v128
	v_exp_f32_e32 v129, v129
	s_add_i32 s6, s42, 0xffffff60
	s_waitcnt lgkmcnt(0)
	v_mfma_f32_32x32x16_bf16 v[86:101], v[8:11], v[174:177], 0
	ds_read_b128 v[4:7], v213 offset:49152
	ds_read_b128 v[8:11], v213 offset:57344
	s_add_i32 s7, s42, 0xffffff9f
	s_waitcnt lgkmcnt(1)
	v_mfma_f32_32x32x16_bf16 v[102:117], v[4:7], v[170:173], v[102:117]
	s_waitcnt lgkmcnt(0)
	v_mfma_f32_32x32x16_bf16 v[86:101], v[8:11], v[170:173], v[86:101]
	ds_read_b128 v[4:7], v214 offset:49152
	ds_read_b128 v[8:11], v214 offset:57344
	s_waitcnt lgkmcnt(1)
	v_mfma_f32_32x32x16_bf16 v[102:117], v[4:7], v[166:169], v[102:117]
	s_waitcnt lgkmcnt(0)
	v_mfma_f32_32x32x16_bf16 v[86:101], v[8:11], v[166:169], v[86:101]
	ds_read_b128 v[4:7], v215 offset:49152
	ds_read_b128 v[8:11], v215 offset:57344
	s_waitcnt lgkmcnt(1)
	v_mfma_f32_32x32x16_bf16 v[102:117], v[4:7], v[162:165], v[102:117]
	s_waitcnt lgkmcnt(0)
	v_mfma_f32_32x32x16_bf16 v[86:101], v[8:11], v[162:165], v[86:101]
	ds_read_b128 v[4:7], v212 offset:49280
	ds_read_b128 v[8:11], v212 offset:57472
	s_waitcnt lgkmcnt(1)
	v_mfma_f32_32x32x16_bf16 v[102:117], v[4:7], v[158:161], v[102:117]
	s_waitcnt lgkmcnt(0)
	v_mfma_f32_32x32x16_bf16 v[86:101], v[8:11], v[158:161], v[86:101]
	ds_read_b128 v[4:7], v213 offset:49280
	ds_read_b128 v[8:11], v213 offset:57472
	s_waitcnt lgkmcnt(1)
	v_mfma_f32_32x32x16_bf16 v[102:117], v[4:7], v[154:157], v[102:117]
	s_waitcnt lgkmcnt(0)
	v_mfma_f32_32x32x16_bf16 v[86:101], v[8:11], v[154:157], v[86:101]
	ds_read_b128 v[4:7], v214 offset:49280
	ds_read_b128 v[8:11], v214 offset:57472
	s_waitcnt lgkmcnt(1)
	v_mfma_f32_32x32x16_bf16 v[102:117], v[4:7], v[150:153], v[102:117]
	s_waitcnt lgkmcnt(0)
	v_mfma_f32_32x32x16_bf16 v[86:101], v[8:11], v[150:153], v[86:101]
	ds_read_b128 v[4:7], v215 offset:49280
	ds_read_b128 v[8:11], v215 offset:57472
	s_waitcnt lgkmcnt(1)
	v_mfma_f32_32x32x16_bf16 v[102:117], v[4:7], v[146:149], v[102:117]
	s_waitcnt lgkmcnt(0)
	v_mfma_f32_32x32x16_bf16 v[86:101], v[8:11], v[146:149], v[86:101]
	v_add_u32_e32 v8, s10, v216
	ds_read_b128 v[4:7], v8
	ds_read_b128 v[8:11], v8 offset:4096
	ds_read_b128 v[12:15], v202
	s_waitcnt lgkmcnt(0)
	v_mfma_f32_32x32x16_bf16 v[102:117], v[4:7], v[12:15], v[102:117]
	v_mfma_f32_32x32x16_bf16 v[86:101], v[8:11], v[12:15], v[86:101]
	v_add_u32_e32 v8, s10, v217
	ds_read_b128 v[4:7], v8
	ds_read_b128 v[8:11], v8 offset:4096
	ds_read_b128 v[12:15], v202 offset:1024
	s_waitcnt lgkmcnt(0)
	v_mfma_f32_32x32x16_bf16 v[102:117], v[4:7], v[12:15], v[102:117]
	v_mfma_f32_32x32x16_bf16 v[86:101], v[8:11], v[12:15], v[86:101]
	v_add_u32_e32 v8, s10, v218
	ds_read_b128 v[4:7], v8
	ds_read_b128 v[8:11], v8 offset:4096
	ds_read_b128 v[12:15], v202 offset:2048
	s_waitcnt lgkmcnt(0)
	v_mfma_f32_32x32x16_bf16 v[102:117], v[4:7], v[12:15], v[102:117]
	v_mfma_f32_32x32x16_bf16 v[86:101], v[8:11], v[12:15], v[86:101]
	v_add_u32_e32 v8, s10, v219
	ds_read_b128 v[4:7], v8
	ds_read_b128 v[8:11], v8 offset:4096
	ds_read_b128 v[12:15], v202 offset:3072
	s_waitcnt lgkmcnt(0)
; __device__ __forceinline__ void finishSM(f32x16& p0, f32x16& p1, float alpha, float& l_reg, bf16x8& pa0, bf16x8& pa1, bf16x8& pa2, bf16x8& pa3) {
; #pragma unroll
;     for (int r = 0; r < 16; ++r) p1[r] = __builtin_amdgcn_exp2f(p1[r]);
;     float ps = 0;
; #pragma unroll
;     for (int r = 0; r < 16; ++r) ps += p0[r];
; #pragma unroll
;     for (int r = 0; r < 16; ++r) ps += p1[r];
;     { auto rr = __builtin_amdgcn_permlane32_swap(__float_as_uint(ps), __float_as_uint(ps), false, false);
;       ps = __uint_as_float(rr[0]) + __uint_as_float(rr[1]); }
;     l_reg = l_reg * alpha + ps;
;     ...
;     PK4(p0, 0, pa0); PK4(p0, 8, pa1); PK4(p1, 0, pa2); PK4(p1, 8, pa3);
;     ...
; }
; template <int VB, bool SK>
; __device__ __forceinline__ void pv_tile(f32x16* o, int vb0, bf16x8 pa0, bf16x8 pa1, bf16x8 pa2, bf16x8 pa3, bool act) {
;     if (SK && !act) return;
;     ...
;     if (ATT_PRIO) __builtin_amdgcn_s_setprio(1);
;     PV_D0(0); PV_D0(1); PV_D0(2); PV_D0(3);
;     if (ATT_PRIO) __builtin_amdgcn_s_setprio(0);
;     ...
; }
	v_mfma_f32_32x32x16_bf16 v[102:117], v[4:7], v[12:15], v[102:117]
	v_exp_f32_e32 v4, v140
	v_exp_f32_e32 v5, v141
	v_exp_f32_e32 v6, v138
	v_exp_f32_e32 v7, v139
	v_mfma_f32_32x32x16_bf16 v[86:101], v[8:11], v[12:15], v[86:101]
	ds_read_b64_tr_b16 v[230:231], v209 offset:0
	ds_read_b64_tr_b16 v[232:233], v209 offset:0x800
	ds_read_b64_tr_b16 v[234:235], v209 offset:0x1000
	ds_read_b64_tr_b16 v[236:237], v209 offset:0x1800
	ds_read_b64_tr_b16 v[238:239], v209 offset:0x2000
	ds_read_b64_tr_b16 v[240:241], v209 offset:0x2800
	ds_read_b64_tr_b16 v[242:243], v209 offset:0x3000
	ds_read_b64_tr_b16 v[244:245], v209 offset:0x3800
	v_add_f32_e32 v12, v227, v188
	v_add_f32_e32 v12, v186, v12
	v_add_f32_e32 v12, v189, v12
	v_add_f32_e32 v12, v185, v12
	v_add_f32_e32 v12, v187, v12
	v_add_f32_e32 v12, v183, v12
	v_add_f32_e32 v12, v184, v12
	v_add_f32_e32 v12, v179, v12
	v_add_f32_e32 v12, v182, v12
	v_add_f32_e32 v12, v144, v12
	v_add_f32_e32 v12, v180, v12
	v_add_f32_e32 v12, v142, v12
	v_add_f32_e32 v12, v181, v12
	v_add_f32_e32 v12, v143, v12
	v_add_f32_e32 v12, v145, v12
	v_exp_f32_e32 v8, v136
	v_add_f32_e32 v12, v4, v12
	v_exp_f32_e32 v9, v137
	v_add_f32_e32 v12, v5, v12
	v_exp_f32_e32 v10, v134
	v_add_f32_e32 v12, v6, v12
	v_exp_f32_e32 v11, v135
	v_add_f32_e32 v12, v7, v12
	v_add_f32_e32 v12, v8, v12
	v_add_f32_e32 v12, v9, v12
	v_add_f32_e32 v12, v10, v12
	v_add_f32_e32 v12, v11, v12
	v_add_f32_e32 v12, v122, v12
	v_add_f32_e32 v12, v123, v12
	v_add_f32_e32 v12, v124, v12
	v_add_f32_e32 v12, v125, v12
	v_add_f32_e32 v12, v126, v12
	v_add_f32_e32 v12, v127, v12
	v_add_f32_e32 v12, v128, v12
	v_add_f32_e32 v195, v129, v12
	v_mov_b32_e32 v225, v195
	s_nop 1
	v_permlane32_swap_b32_e32 v195, v225
	v_cvt_pk_bf16_f32 v12, v188, v227
	v_cvt_pk_bf16_f32 v13, v186, v189
	v_cvt_pk_bf16_f32 v14, v185, v187
	v_cvt_pk_bf16_f32 v15, v183, v184
	v_cvt_pk_bf16_f32 v82, v179, v182
	v_cvt_pk_bf16_f32 v83, v144, v180
	v_cvt_pk_bf16_f32 v84, v142, v181
	v_cvt_pk_bf16_f32 v85, v143, v145
	v_cvt_pk_bf16_f32 v118, v4, v5
	v_cvt_pk_bf16_f32 v119, v6, v7
	v_cvt_pk_bf16_f32 v120, v8, v9
	v_cvt_pk_bf16_f32 v121, v10, v11
	v_cvt_pk_bf16_f32 v122, v122, v123
	v_cvt_pk_bf16_f32 v123, v124, v125
	v_cvt_pk_bf16_f32 v124, v126, v127
	v_cvt_pk_bf16_f32 v125, v128, v129
	s_nop 0
	v_permlane32_swap_b32_e32 v12, v14
	v_permlane32_swap_b32_e32 v13, v15
	v_permlane32_swap_b32_e32 v82, v84
	v_permlane32_swap_b32_e32 v83, v85
	v_permlane32_swap_b32_e32 v118, v120
	v_permlane32_swap_b32_e32 v119, v121
	v_permlane32_swap_b32_e32 v122, v124
	v_permlane32_swap_b32_e32 v123, v125
	s_add_i32 s10, s42, 0xffffffa0
	s_sub_i32 s64, s42, 64
	s_mov_b32 s65, s11
	s_lshl_b64 s[44:45], s[10:11], 12
	s_lshl_b64 s[64:65], s[64:65], 12
	v_lshl_add_u64 v[4:5], v[196:197], 0, s[44:45]
	v_lshl_add_u64 v[8:9], v[196:197], 0, s[64:65]
	v_lshl_add_u64 v[126:127], v[198:199], 0, s[44:45]
	s_add_i32 m0, s37, 0x8000
	global_load_dwordx4 v[4:7], v[4:5], off
	s_nop 0
	global_load_dwordx4 v[8:11], v[8:9], off
	s_lshl_b64 s[44:45], s[10:11], 7
	global_load_lds_dwordx4 v[126:127], off
	v_lshl_add_u64 v[126:127], v[198:199], 0, s[64:65]
	s_add_i32 m0, s37, 0xa000
	s_nop 0
	global_load_lds_dwordx4 v[126:127], off
	v_lshl_add_u64 v[126:127], v[16:17], 0, s[44:45]
	s_add_i32 m0, s37, 0x10800
	s_nop 0
	global_load_lds_dwordx4 v[126:127], off
	s_waitcnt lgkmcnt(0)
	s_nop 0
	v_mfma_f32_32x32x16_bf16 v[66:81], v[12:15], v[230:233], v[66:81]
	ds_read_b64_tr_b16 v[126:127], v209 offset:0x200
	ds_read_b64_tr_b16 v[128:129], v209 offset:0xa00
	v_mfma_f32_32x32x16_bf16 v[66:81], v[82:85], v[234:237], v[66:81]
	ds_read_b64_tr_b16 v[130:131], v209 offset:0x1200
	ds_read_b64_tr_b16 v[132:133], v209 offset:0x1a00
	v_mfma_f32_32x32x16_bf16 v[66:81], v[118:121], v[238:241], v[66:81]
	ds_read_b64_tr_b16 v[134:135], v209 offset:0x2200
	ds_read_b64_tr_b16 v[136:137], v209 offset:0x2a00
	ds_read_b64_tr_b16 v[142:143], v209 offset:0x3200
	ds_read_b64_tr_b16 v[144:145], v209 offset:0x3a00
	s_waitcnt lgkmcnt(0)
	v_mfma_f32_32x32x16_bf16 v[66:81], v[122:125], v[242:245], v[66:81]
	v_mfma_f32_32x32x16_bf16 v[50:65], v[12:15], v[126:129], v[50:65]
	ds_read_b64_tr_b16 v[126:127], v209 offset:0x400
	ds_read_b64_tr_b16 v[128:129], v209 offset:0xc00
	v_mfma_f32_32x32x16_bf16 v[50:65], v[82:85], v[130:133], v[50:65]
	ds_read_b64_tr_b16 v[130:131], v209 offset:0x1400
	ds_read_b64_tr_b16 v[132:133], v209 offset:0x1c00
	v_mfma_f32_32x32x16_bf16 v[50:65], v[118:121], v[134:137], v[50:65]
	ds_read_b64_tr_b16 v[134:135], v209 offset:0x2400
	ds_read_b64_tr_b16 v[136:137], v209 offset:0x2c00
	ds_read_b64_tr_b16 v[138:139], v209 offset:0x3400
	ds_read_b64_tr_b16 v[140:141], v209 offset:0x3c00
	s_waitcnt lgkmcnt(0)
	v_mfma_f32_32x32x16_bf16 v[50:65], v[122:125], v[142:145], v[50:65]
	v_mfma_f32_32x32x16_bf16 v[34:49], v[12:15], v[126:129], v[34:49]
	ds_read_b64_tr_b16 v[126:127], v209 offset:0x600
	ds_read_b64_tr_b16 v[128:129], v209 offset:0xe00
	v_mfma_f32_32x32x16_bf16 v[34:49], v[82:85], v[130:133], v[34:49]
	ds_read_b64_tr_b16 v[130:131], v209 offset:0x1600
	ds_read_b64_tr_b16 v[132:133], v209 offset:0x1e00
	v_mfma_f32_32x32x16_bf16 v[34:49], v[118:121], v[134:137], v[34:49]
	ds_read_b64_tr_b16 v[134:135], v209 offset:0x2600
	ds_read_b64_tr_b16 v[136:137], v209 offset:0x2e00
	ds_read_b64_tr_b16 v[142:143], v209 offset:0x3600
	ds_read_b64_tr_b16 v[144:145], v209 offset:0x3e00
	s_waitcnt lgkmcnt(0)
	v_mfma_f32_32x32x16_bf16 v[34:49], v[122:125], v[138:141], v[34:49]
	v_mfma_f32_32x32x16_bf16 v[18:33], v[12:15], v[126:129], v[18:33]
	s_cmp_le_i32 s7, s40
	s_cselect_b64 s[44:45], -1, 0
	s_cmp_gt_i32 s6, s60
	s_cselect_b64 s[6:7], -1, 0
	s_and_b64 s[6:7], s[6:7], s[44:45]
	s_and_b64 vcc, exec, s[6:7]
	v_mfma_f32_32x32x16_bf16 v[18:33], v[82:85], v[130:133], v[18:33]
	v_mfma_f32_32x32x16_bf16 v[18:33], v[118:121], v[134:137], v[18:33]
	v_mfma_f32_32x32x16_bf16 v[18:33], v[122:125], v[142:145], v[18:33]
	s_cbranch_vccnz .LBB0_1038
; __device__ __forceinline__ void mask_tile(f32x16& p0, f32x16& p1, int dq, unsigned W) {
;     const float NEG = -__builtin_inff();
; #pragma unroll
;     for (int r = 0; r < 16; ++r) {
;         const int c = (r & 3) + 8 * (r >> 2);
;         if ((unsigned)(dq - c) >= W) p0[r] = NEG;
;         if ((unsigned)(dq - c - 32) >= W) p1[r] = NEG;
;     }
; }
	v_add_u32_e32 v12, 0x7b, v193
	v_cmp_gt_u32_e32 vcc, 2.0, v12
	v_add_u32_e32 v12, 0x5b, v193
	s_nop 0
	v_cndmask_b32_e32 v102, v200, v102, vcc
	v_cmp_gt_u32_e32 vcc, 2.0, v12
	v_add_u32_e32 v12, 0x7a, v193
	s_nop 0
	v_cndmask_b32_e32 v86, v200, v86, vcc
	v_cmp_gt_u32_e32 vcc, 2.0, v12
	v_add_u32_e32 v12, 0x5a, v193
	s_nop 0
	v_cndmask_b32_e32 v103, v200, v103, vcc
	v_cmp_gt_u32_e32 vcc, 2.0, v12
	v_add_u32_e32 v12, 0x79, v193
	s_nop 0
	v_cndmask_b32_e32 v87, v200, v87, vcc
	v_cmp_gt_u32_e32 vcc, 2.0, v12
	v_add_u32_e32 v12, 0x59, v193
	s_nop 0
	v_cndmask_b32_e32 v104, v200, v104, vcc
	v_cmp_gt_u32_e32 vcc, 2.0, v12
	v_add_u32_e32 v12, 0x78, v193
	s_nop 0
	v_cndmask_b32_e32 v88, v200, v88, vcc
	v_cmp_gt_u32_e32 vcc, 2.0, v12
	v_add_u32_e32 v12, 0x58, v193
	s_nop 0
	v_cndmask_b32_e32 v105, v200, v105, vcc
	v_cmp_gt_u32_e32 vcc, 2.0, v12
	v_add_u32_e32 v12, 0x73, v193
	s_nop 0
	v_cndmask_b32_e32 v89, v200, v89, vcc
	v_cmp_gt_u32_e32 vcc, 2.0, v12
	v_add_u32_e32 v12, 0x53, v193
	s_nop 0
	v_cndmask_b32_e32 v106, v200, v106, vcc
	v_cmp_gt_u32_e32 vcc, 2.0, v12
	v_add_u32_e32 v12, 0x72, v193
	s_nop 0
	v_cndmask_b32_e32 v90, v200, v90, vcc
	v_cmp_gt_u32_e32 vcc, 2.0, v12
	v_add_u32_e32 v12, 0x52, v193
	s_nop 0
	v_cndmask_b32_e32 v107, v200, v107, vcc
	v_cmp_gt_u32_e32 vcc, 2.0, v12
	v_add_u32_e32 v12, 0x71, v193
	s_nop 0
	v_cndmask_b32_e32 v91, v200, v91, vcc
	v_cmp_gt_u32_e32 vcc, 2.0, v12
	v_add_u32_e32 v12, 0x51, v193
	s_nop 0
	v_cndmask_b32_e32 v108, v200, v108, vcc
	v_cmp_gt_u32_e32 vcc, 2.0, v12
	v_add_u32_e32 v12, 0x70, v193
	s_nop 0
	v_cndmask_b32_e32 v92, v200, v92, vcc
	v_cmp_gt_u32_e32 vcc, 2.0, v12
	v_add_u32_e32 v12, 0x50, v193
	s_nop 0
	v_cndmask_b32_e32 v109, v200, v109, vcc
	v_cmp_gt_u32_e32 vcc, 2.0, v12
	v_add_u32_e32 v12, 0x6b, v193
	s_nop 0
	v_cndmask_b32_e32 v93, v200, v93, vcc
	v_cmp_gt_u32_e32 vcc, 2.0, v12
	v_add_u32_e32 v12, 0x4b, v193
	s_nop 0
	v_cndmask_b32_e32 v110, v200, v110, vcc
	v_cmp_gt_u32_e32 vcc, 2.0, v12
	v_add_u32_e32 v12, 0x6a, v193
	s_nop 0
	v_cndmask_b32_e32 v94, v200, v94, vcc
	v_cmp_gt_u32_e32 vcc, 2.0, v12
	v_add_u32_e32 v12, 0x4a, v193
	s_nop 0
	v_cndmask_b32_e32 v111, v200, v111, vcc
	v_cmp_gt_u32_e32 vcc, 2.0, v12
	v_add_u32_e32 v12, 0x69, v193
	s_nop 0
	v_cndmask_b32_e32 v95, v200, v95, vcc
	v_cmp_gt_u32_e32 vcc, 2.0, v12
	v_add_u32_e32 v12, 0x49, v193
	s_nop 0
	v_cndmask_b32_e32 v112, v200, v112, vcc
	v_cmp_gt_u32_e32 vcc, 2.0, v12
	v_add_u32_e32 v12, 0x68, v193
	s_nop 0
	v_cndmask_b32_e32 v96, v200, v96, vcc
	v_cmp_gt_u32_e32 vcc, 2.0, v12
	v_add_u32_e32 v12, 0x48, v193
	s_nop 0
	v_cndmask_b32_e32 v113, v200, v113, vcc
	v_cmp_gt_u32_e32 vcc, 2.0, v12
	v_add_u32_e32 v12, 0x63, v193
	s_nop 0
	v_cndmask_b32_e32 v97, v200, v97, vcc
	v_cmp_gt_u32_e32 vcc, 2.0, v12
	v_add_u32_e32 v12, 0x43, v193
	s_nop 0
	v_cndmask_b32_e32 v114, v200, v114, vcc
	v_cmp_gt_u32_e32 vcc, 2.0, v12
	v_add_u32_e32 v12, 0x62, v193
	s_nop 0
	v_cndmask_b32_e32 v98, v200, v98, vcc
	v_cmp_gt_u32_e32 vcc, 2.0, v12
	v_add_u32_e32 v12, 0x42, v193
	s_nop 0
	v_cndmask_b32_e32 v115, v200, v115, vcc
	v_cmp_gt_u32_e32 vcc, 2.0, v12
	v_add_u32_e32 v12, 0x61, v193
	s_nop 0
	v_cndmask_b32_e32 v99, v200, v99, vcc
	v_cmp_gt_u32_e32 vcc, 2.0, v12
	v_add_u32_e32 v12, 0x41, v193
	s_nop 0
	v_cndmask_b32_e32 v116, v200, v116, vcc
	v_cmp_gt_u32_e32 vcc, 2.0, v12
	v_add_u32_e32 v12, 0x60, v193
	s_nop 0
	v_cndmask_b32_e32 v100, v200, v100, vcc
	v_cmp_gt_u32_e32 vcc, 2.0, v12
	v_add_u32_e32 v12, 64, v193
	s_nop 0
	v_cndmask_b32_e32 v117, v200, v117, vcc
	v_cmp_gt_u32_e32 vcc, 2.0, v12
	s_nop 1
	v_cndmask_b32_e32 v101, v200, v101, vcc

; template <int MODE>
; __device__ __forceinline__ void partialSM(f32x16& p0, f32x16& p1, float& m_reg, float& mn, float& alpha) {
;     constexpr float SCALE = Cfg<MODE>::SCALE;
;     float pmax = p0[0];
; #pragma unroll
;     for (int r = 1; r < 16; ++r) pmax = fmaxf(pmax, p0[r]);
; #pragma unroll
;     for (int r = 0; r < 16; ++r) pmax = fmaxf(pmax, p1[r]);
;     { auto rr = __builtin_amdgcn_permlane32_swap(__float_as_uint(pmax), __float_as_uint(pmax), false, false);
;       pmax = fmaxf(__uint_as_float(rr[0]), __uint_as_float(rr[1])); }
;     constexpr float C2 = 1.4426950408889634f * SCALE;
;     if (__builtin_expect(__all((pmax - m_reg) * SCALE <= THR), 1)) { mn = m_reg; alpha = 1.f; }
;     else { mn = fmaxf(m_reg, pmax); alpha = __builtin_amdgcn_exp2f((m_reg - mn) * C2); m_reg = mn; }
;     const float mnL = -mn * C2;
; #pragma unroll
;     for (int r = 0; r < 16; ++r) p0[r] = fmaf(p0[r], C2, mnL);
; #pragma unroll
;     for (int r = 0; r < 16; ++r) p1[r] = fmaf(p1[r], C2, mnL);
; #pragma unroll
;     for (int r = 0; r < 16; ++r) p0[r] = __builtin_amdgcn_exp2f(p0[r]);
; }
; template <int KB, bool SK, bool ROPE, bool QHALF>
; __device__ __forceinline__ void qkt(f32x16& p0, f32x16& p1, const char* lds, int r32, int hi, const bf16x8* qr, const char* qrl, bool act) {
;     if (SK && !act) { const float NEG = -__builtin_inff();
; #pragma unroll
;         for (int r = 0; r < 16; ++r) { p0[r] = NEG; p1[r] = NEG; } return; }
;     p0 = f32x16{}; p1 = f32x16{};
;     ...
;     if (ATT_PRIO) __builtin_amdgcn_s_setprio(1);
;     const char* kb[4];
; #pragma unroll
;     for (int dd = 0; dd < 4; ++dd) kb[dd] = lds + OFF_K + KB * SHM_K + KSWZ(r32, (dd * 16 + hi * 8) * 2);
; #pragma unroll
;     for (int d0 = 0; d0 < 8; ++d0) { const char* a = kb[d0 & 3] + (d0 >> 2) * 128;
;         bf16x8 b0 = *reinterpret_cast<const bf16x8*>(a);
;         bf16x8 b1 = *reinterpret_cast<const bf16x8*>(a + 32 * 256);
;         bf16x8 qf;
;         if constexpr (QHALF) { if (d0 >= 4) qf = *reinterpret_cast<const bf16x8*>(qrl + (d0 - 4) * 1024); else qf = qr[d0]; } else qf = qr[d0];
;         p0 = __builtin_amdgcn_mfma_f32_32x32x16_bf16(b0, qf, p0, 0, 0, 0);
;         p1 = __builtin_amdgcn_mfma_f32_32x32x16_bf16(b1, qf, p1, 0, 0, 0); }
.LBB0_1042:
	v_cndmask_b32_e64 v227, v12, v178, s[6:7]
	v_mul_f32_e32 v12, 0xbdd53b94, v227
	v_fmamk_f32 v82, v102, 0x3dd53b94, v12
	v_fmamk_f32 v83, v103, 0x3dd53b94, v12
	v_fmamk_f32 v84, v104, 0x3dd53b94, v12
	v_fmamk_f32 v85, v105, 0x3dd53b94, v12
	v_fmamk_f32 v118, v106, 0x3dd53b94, v12
	v_fmamk_f32 v119, v107, 0x3dd53b94, v12
	v_fmamk_f32 v120, v108, 0x3dd53b94, v12
	v_fmamk_f32 v121, v109, 0x3dd53b94, v12
	v_fmamk_f32 v122, v110, 0x3dd53b94, v12
	v_fmamk_f32 v123, v111, 0x3dd53b94, v12
	v_fmamk_f32 v112, v112, 0x3dd53b94, v12
	v_fmamk_f32 v113, v113, 0x3dd53b94, v12
	v_fmamk_f32 v114, v114, 0x3dd53b94, v12
	v_fmamk_f32 v115, v115, 0x3dd53b94, v12
	v_fmamk_f32 v116, v116, 0x3dd53b94, v12
	v_fmamk_f32 v117, v117, 0x3dd53b94, v12
	v_fmamk_f32 v102, v86, 0x3dd53b94, v12
	v_fmamk_f32 v103, v87, 0x3dd53b94, v12
	v_fmamk_f32 v104, v88, 0x3dd53b94, v12
	v_fmamk_f32 v110, v89, 0x3dd53b94, v12
	v_fmamk_f32 v111, v90, 0x3dd53b94, v12
	v_fmamk_f32 v14, v91, 0x3dd53b94, v12
	v_fmamk_f32 v15, v92, 0x3dd53b94, v12
	v_fmamk_f32 v105, v93, 0x3dd53b94, v12
	v_fmamk_f32 v106, v94, 0x3dd53b94, v12
	v_fmamk_f32 v107, v95, 0x3dd53b94, v12
	v_fmamk_f32 v108, v96, 0x3dd53b94, v12
	v_fmamk_f32 v109, v97, 0x3dd53b94, v12
	v_exp_f32_e32 v82, v82
	v_exp_f32_e32 v83, v83
	v_exp_f32_e32 v84, v84
	v_exp_f32_e32 v85, v85
	v_exp_f32_e32 v86, v118
	v_exp_f32_e32 v87, v119
	v_exp_f32_e32 v88, v120
	v_exp_f32_e32 v89, v121
	v_exp_f32_e32 v90, v122
	v_exp_f32_e32 v91, v123
	v_exp_f32_e32 v92, v112
	v_exp_f32_e32 v93, v113
	v_exp_f32_e32 v94, v114
	v_exp_f32_e32 v95, v115
	v_exp_f32_e32 v96, v116
	v_exp_f32_e32 v97, v117
	v_fmamk_f32 v13, v98, 0x3dd53b94, v12
	v_fmamk_f32 v112, v99, 0x3dd53b94, v12
	v_fmamk_f32 v113, v100, 0x3dd53b94, v12
	v_fmac_f32_e32 v12, 0x3dd53b94, v101
	s_waitcnt lgkmcnt(0)
	ds_read_b128 v[98:101], v212 offset:32768
	ds_read_b128 v[114:117], v212 offset:40960
	v_exp_f32_e32 v105, v105
	v_exp_f32_e32 v106, v106
	v_exp_f32_e32 v107, v107
	s_waitcnt lgkmcnt(1)
	v_mfma_f32_32x32x16_bf16 v[130:145], v[98:101], v[174:177], 0
	ds_read_b128 v[98:101], v213 offset:32768
	ds_read_b128 v[178:181], v213 offset:40960
	v_exp_f32_e32 v108, v108
	v_exp_f32_e32 v109, v109
	s_waitcnt lgkmcnt(2)
	v_mfma_f32_32x32x16_bf16 v[114:129], v[114:117], v[174:177], 0
	s_waitcnt lgkmcnt(1)
	v_mfma_f32_32x32x16_bf16 v[130:145], v[98:101], v[170:173], v[130:145]
	s_waitcnt lgkmcnt(0)
	v_mfma_f32_32x32x16_bf16 v[114:129], v[178:181], v[170:173], v[114:129]
	ds_read_b128 v[98:101], v214 offset:32768
	ds_read_b128 v[178:181], v214 offset:40960
	s_waitcnt lgkmcnt(1)
	v_mfma_f32_32x32x16_bf16 v[130:145], v[98:101], v[166:169], v[130:145]
	s_waitcnt lgkmcnt(0)
	v_mfma_f32_32x32x16_bf16 v[114:129], v[178:181], v[166:169], v[114:129]
	ds_read_b128 v[98:101], v215 offset:32768
	ds_read_b128 v[178:181], v215 offset:40960
	s_waitcnt lgkmcnt(1)
	v_mfma_f32_32x32x16_bf16 v[130:145], v[98:101], v[162:165], v[130:145]
	s_waitcnt lgkmcnt(0)
	v_mfma_f32_32x32x16_bf16 v[114:129], v[178:181], v[162:165], v[114:129]
	ds_read_b128 v[98:101], v212 offset:32896
	ds_read_b128 v[178:181], v212 offset:41088
	s_waitcnt lgkmcnt(1)
	v_mfma_f32_32x32x16_bf16 v[130:145], v[98:101], v[158:161], v[130:145]
	s_waitcnt lgkmcnt(0)
	v_mfma_f32_32x32x16_bf16 v[114:129], v[178:181], v[158:161], v[114:129]
	ds_read_b128 v[98:101], v213 offset:32896
	ds_read_b128 v[178:181], v213 offset:41088
	s_waitcnt lgkmcnt(1)
	v_mfma_f32_32x32x16_bf16 v[130:145], v[98:101], v[154:157], v[130:145]
	s_waitcnt lgkmcnt(0)
	v_mfma_f32_32x32x16_bf16 v[114:129], v[178:181], v[154:157], v[114:129]
	ds_read_b128 v[98:101], v214 offset:32896
	ds_read_b128 v[178:181], v214 offset:41088
	s_waitcnt lgkmcnt(1)
	v_mfma_f32_32x32x16_bf16 v[130:145], v[98:101], v[150:153], v[130:145]
	s_waitcnt lgkmcnt(0)
	v_mfma_f32_32x32x16_bf16 v[114:129], v[178:181], v[150:153], v[114:129]
	ds_read_b128 v[98:101], v215 offset:32896
	ds_read_b128 v[178:181], v215 offset:41088
	s_waitcnt lgkmcnt(1)
	v_mfma_f32_32x32x16_bf16 v[130:145], v[98:101], v[146:149], v[130:145]
	s_waitcnt lgkmcnt(0)
	v_mfma_f32_32x32x16_bf16 v[114:129], v[178:181], v[146:149], v[114:129]
	ds_read_b128 v[98:101], v221
	ds_read_b128 v[178:181], v221 offset:4096
	ds_read_b128 v[182:185], v202
	s_waitcnt lgkmcnt(0)
; __device__ __forceinline__ void finishSM(f32x16& p0, f32x16& p1, float alpha, float& l_reg, bf16x8& pa0, bf16x8& pa1, bf16x8& pa2, bf16x8& pa3) {
; #pragma unroll
;     for (int r = 0; r < 16; ++r) p1[r] = __builtin_amdgcn_exp2f(p1[r]);
;     float ps = 0;
; #pragma unroll
;     for (int r = 0; r < 16; ++r) ps += p0[r];
; #pragma unroll
;     for (int r = 0; r < 16; ++r) ps += p1[r];
;     { auto rr = __builtin_amdgcn_permlane32_swap(__float_as_uint(ps), __float_as_uint(ps), false, false);
;       ps = __uint_as_float(rr[0]) + __uint_as_float(rr[1]); }
;     l_reg = l_reg * alpha + ps;
;     ...
;     PK4(p0, 0, pa0); PK4(p0, 8, pa1); PK4(p1, 0, pa2); PK4(p1, 8, pa3);
;     ...
; }
	v_mfma_f32_32x32x16_bf16 v[130:145], v[98:101], v[182:185], v[130:145]
	v_mfma_f32_32x32x16_bf16 v[114:129], v[178:181], v[182:185], v[114:129]
	ds_read_b128 v[98:101], v222
	ds_read_b128 v[178:181], v222 offset:4096
	ds_read_b128 v[182:185], v202 offset:1024
	s_waitcnt lgkmcnt(0)
	v_mfma_f32_32x32x16_bf16 v[130:145], v[98:101], v[182:185], v[130:145]
	v_mfma_f32_32x32x16_bf16 v[114:129], v[178:181], v[182:185], v[114:129]
	ds_read_b128 v[98:101], v223
	ds_read_b128 v[178:181], v223 offset:4096
	ds_read_b128 v[182:185], v202 offset:2048
	s_waitcnt lgkmcnt(0)
	v_mfma_f32_32x32x16_bf16 v[130:145], v[98:101], v[182:185], v[130:145]
	v_mfma_f32_32x32x16_bf16 v[114:129], v[178:181], v[182:185], v[114:129]
	ds_read_b128 v[98:101], v224
	ds_read_b128 v[178:181], v224 offset:4096
	ds_read_b128 v[182:185], v202 offset:3072
	s_waitcnt lgkmcnt(0)
	v_mfma_f32_32x32x16_bf16 v[130:145], v[98:101], v[182:185], v[130:145]
	ds_read_b64_tr_b16 v[230:231], v209 offset:0x4000
	ds_read_b64_tr_b16 v[232:233], v209 offset:0x4800
	ds_read_b64_tr_b16 v[234:235], v209 offset:0x5000
	ds_read_b64_tr_b16 v[236:237], v209 offset:0x5800
	ds_read_b64_tr_b16 v[238:239], v209 offset:0x6000
	ds_read_b64_tr_b16 v[240:241], v209 offset:0x6800
	ds_read_b64_tr_b16 v[242:243], v209 offset:0x7000
	ds_read_b64_tr_b16 v[244:245], v209 offset:0x7800
	v_exp_f32_e32 v98, v102
	v_exp_f32_e32 v102, v111
	v_exp_f32_e32 v111, v112
	v_exp_f32_e32 v112, v113
	v_exp_f32_e32 v113, v12
	v_add_f32_e32 v12, v83, v82
	v_add_f32_e32 v12, v84, v12
	v_add_f32_e32 v12, v85, v12
	v_add_f32_e32 v12, v86, v12
	v_add_f32_e32 v12, v87, v12
	v_add_f32_e32 v12, v88, v12
	v_add_f32_e32 v12, v89, v12
	v_add_f32_e32 v12, v90, v12
	v_add_f32_e32 v12, v91, v12
	v_add_f32_e32 v12, v92, v12
	v_add_f32_e32 v12, v93, v12
	v_add_f32_e32 v12, v94, v12
	v_exp_f32_e32 v99, v103
	v_add_f32_e32 v12, v95, v12
	v_exp_f32_e32 v100, v104
	v_add_f32_e32 v12, v96, v12
	v_exp_f32_e32 v101, v110
	v_add_f32_e32 v12, v97, v12
	v_add_f32_e32 v12, v98, v12
	v_exp_f32_e32 v103, v14
	v_add_f32_e32 v12, v99, v12
	v_exp_f32_e32 v104, v15
	v_add_f32_e32 v12, v100, v12
	v_add_f32_e32 v12, v101, v12
	v_add_f32_e32 v12, v102, v12
	v_add_f32_e32 v12, v103, v12
	v_add_f32_e32 v12, v104, v12
	v_add_f32_e32 v12, v105, v12
	v_exp_f32_e32 v110, v13
	v_add_f32_e32 v12, v106, v12
	v_add_f32_e32 v12, v107, v12
	v_mfma_f32_32x32x16_bf16 v[114:129], v[178:181], v[182:185], v[114:129]
	v_add_f32_e32 v12, v108, v12
	v_add_f32_e32 v12, v109, v12
	v_add_f32_e32 v12, v110, v12
	v_add_f32_e32 v12, v111, v12
	v_add_f32_e32 v12, v112, v12
	v_add_f32_e32 v228, v113, v12
	v_mov_b32_e32 v229, v228
	v_cvt_pk_bf16_f32 v12, v82, v83
	v_cvt_pk_bf16_f32 v13, v84, v85
	v_cvt_pk_bf16_f32 v14, v86, v87
	v_cvt_pk_bf16_f32 v15, v88, v89
	v_cvt_pk_bf16_f32 v178, v90, v91
	v_cvt_pk_bf16_f32 v179, v92, v93
	v_cvt_pk_bf16_f32 v180, v94, v95
	v_cvt_pk_bf16_f32 v181, v96, v97
	v_cvt_pk_bf16_f32 v182, v98, v99
	v_cvt_pk_bf16_f32 v183, v100, v101
	v_cvt_pk_bf16_f32 v184, v102, v103
	v_cvt_pk_bf16_f32 v185, v104, v105
	v_cvt_pk_bf16_f32 v186, v106, v107
	v_cvt_pk_bf16_f32 v187, v108, v109
	v_cvt_pk_bf16_f32 v188, v110, v111
	v_cvt_pk_bf16_f32 v189, v112, v113
	s_nop 1
	v_permlane32_swap_b32_e32 v228, v229
	v_permlane32_swap_b32_e32 v12, v14
	v_permlane32_swap_b32_e32 v13, v15
	v_permlane32_swap_b32_e32 v178, v180
	v_permlane32_swap_b32_e32 v179, v181
	v_permlane32_swap_b32_e32 v182, v184
	v_permlane32_swap_b32_e32 v183, v185
	v_permlane32_swap_b32_e32 v186, v188
	v_permlane32_swap_b32_e32 v187, v189
	s_add_i32 s6, s36, 1
	s_cmp_lt_i32 s6, s63
	s_cselect_b64 s[44:45], -1, 0
	s_cmp_ge_i32 s6, s63
	s_cbranch_scc1 .LBB0_1044
	s_sub_i32 s6, s42, 32
	s_mov_b32 s7, s11
	s_mov_b32 s43, s11
	s_lshl_b64 s[64:65], s[6:7], 12
	s_lshl_b64 s[66:67], s[42:43], 12
	v_lshl_add_u64 v[4:5], v[196:197], 0, s[64:65]
	v_lshl_add_u64 v[8:9], v[196:197], 0, s[66:67]
	v_lshl_add_u64 v[246:247], v[198:199], 0, s[64:65]
	s_add_i32 m0, s37, 0xc000
	global_load_dwordx4 v[4:7], v[4:5], off
	s_nop 0
	global_load_dwordx4 v[8:11], v[8:9], off
	s_lshl_b64 s[6:7], s[6:7], 7
	global_load_lds_dwordx4 v[246:247], off
	v_lshl_add_u64 v[246:247], v[198:199], 0, s[66:67]
	s_add_i32 m0, s37, 0xe000
	s_nop 0
	global_load_lds_dwordx4 v[246:247], off
	v_lshl_add_u64 v[246:247], v[16:17], 0, s[6:7]
	s_add_i32 m0, s37, 0x12800
	s_nop 0
	global_load_lds_dwordx4 v[246:247], off

; #define SBAR() __builtin_amdgcn_sched_barrier(0)
; #define RESC(a) do { if (__any((a) < 1.f)) { if (hi == 0) al_l[r32] = (a); asm volatile("s_waitcnt lgkmcnt(0)" ::: "memory");              \
;                      _Pragma("unroll") for (int d_ = 0; d_ < 4; ++d_) _Pragma("unroll") for (int r = 0; r < 16; ++r) o[d_][r] *= al_l[crow(r, hi)]; } } while (0)
; #define ACT(t) (KBASE(t) <= qlo + QBLK - 1 && KBASE(t) + KVBLK - 1 >= qlo - W + 1)
; #define RESC(a) do { if (__any((a) < 1.f)) { if (hi == 0) al_l[r32] = (a); asm volatile("s_waitcnt lgkmcnt(0)" ::: "memory");              \
;                      _Pragma("unroll") for (int d_ = 0; d_ < 4; ++d_) _Pragma("unroll") for (int r = 0; r < 16; ++r) o[d_][r] *= al_l[crow(r, hi)]; } } while (0)
; #define ACT(t) (KBASE(t) <= qlo + QBLK - 1 && KBASE(t) + KVBLK - 1 >= qlo - W + 1)
; #define ACT(t) (KBASE(t) <= qlo + QBLK - 1 && KBASE(t) + KVBLK - 1 >= qlo - W + 1)
; __device__ __forceinline__ void finishSM(f32x16& p0, f32x16& p1, float alpha, float& l_reg, bf16x8& pa0, bf16x8& pa1, bf16x8& pa2, bf16x8& pa3) {
; #pragma unroll
;     for (int r = 0; r < 16; ++r) p1[r] = __builtin_amdgcn_exp2f(p1[r]);
;     float ps = 0;
; #pragma unroll
;     for (int r = 0; r < 16; ++r) ps += p0[r];
; #pragma unroll
;     for (int r = 0; r < 16; ++r) ps += p1[r];
;     { auto rr = __builtin_amdgcn_permlane32_swap(__float_as_uint(ps), __float_as_uint(ps), false, false);
;       ps = __uint_as_float(rr[0]) + __uint_as_float(rr[1]); }
;     l_reg = l_reg * alpha + ps;
;     ...
;     PK4(p0, 0, pa0); PK4(p0, 8, pa1); PK4(p1, 0, pa2); PK4(p1, 8, pa3);
;     ...
; }
; template <int MODE>
; __device__ __forceinline__ void attn_block_pipe(const BlockRef& cur, const BlockRef& nxt, char* lds, LAS unsigned char* ldsl, Seam<MODE>& S) {
;     ...
;     SLOAD_H(nxt, kbn, 0); SBAR();
;     QLOAD(nxt);
;     SBAR();
;     finishSM(pA0, pA1, alA, l_reg, pa0, pa1, pa2, pa3); SBAR();
;     PPV<0, SK>(o, vb0, pa0, pa1, pa2, pa3, ACT(even ? NT - 2 : NT - 1));
;     if (even) { MASKT(pB0, pB1, NT - 1, 1); partialSM<MODE>(pB0, pB1, m_reg, mnB, alB); __syncthreads(); RESC(alB);
;         finishSM(pB0, pB1, alB, l_reg, pa0, pa1, pa2, pa3); SBAR(); PPV<1, SK>(o, vb0, pa0, pa1, pa2, pa3, ACT(NT - 1)); }
.LBB0_1054:
	s_add_i32 s6, s59, 0xc0000001
	s_and_b32 s6, s6, 0xffffff00
	s_cmp_gt_i32 s59, 0x3fffffff
	s_cselect_b32 s10, s6, 0
	s_lshl_b64 s[6:7], s[10:11], 12
	s_add_u32 s36, s22, s6
	s_addc_u32 s37, s23, s7
	s_or_b32 s42, s10, 32
	s_mov_b32 s43, s11
	s_lshl_b64 s[42:43], s[42:43], 12
	s_add_u32 s44, s22, s42
	s_addc_u32 s45, s23, s43
	global_load_dwordx4 v[114:117], v194, s[36:37]
	global_load_dwordx4 v[118:121], v194, s[44:45]
	s_lshl_b32 s36, s61, 10
	s_add_i32 s36, s36, 0
	s_add_i32 m0, s36, 0x8000
	s_add_u32 s6, s18, s6
	s_addc_u32 s7, s19, s7
	global_load_lds_dwordx4 v192, s[6:7]
	s_add_i32 m0, s36, 0xa000
	s_add_u32 s6, s18, s42
	s_addc_u32 s7, s19, s43
	global_load_lds_dwordx4 v192, s[6:7]
	s_add_i32 m0, s36, 0x10800
	s_lshl_b64 s[6:7], s[10:11], 7
	s_add_u32 s6, s8, s6
	s_addc_u32 s7, s9, s7
	global_load_lds_dwordx4 v190, s[6:7]
	s_add_i32 s6, s62, s59
	s_mul_i32 s36, s6, 0xc00
	v_mul_u32_u24_e32 v2, 0xc00, v205
	s_mul_hi_i32 s10, s6, 0xc00
	s_add_u32 s6, s53, s36
	v_or_b32_e32 v2, v211, v2
	s_addc_u32 s7, s55, s10
	global_load_dwordx4 v[174:177], v2, s[6:7]
	global_load_dwordx4 v[170:173], v2, s[6:7] offset:32
	global_load_dwordx4 v[166:169], v2, s[6:7] offset:64
	global_load_dwordx4 v[162:165], v2, s[6:7] offset:96
	global_load_dwordx4 v[158:161], v2, s[6:7] offset:128
	global_load_dwordx4 v[154:157], v2, s[6:7] offset:160
	global_load_dwordx4 v[150:153], v2, s[6:7] offset:192
	global_load_dwordx4 v[146:149], v2, s[6:7] offset:224
	s_add_u32 s6, s27, s36
	s_addc_u32 s7, s54, s10
	global_load_dwordx4 v[4:7], v2, s[6:7]
	global_load_dwordx4 v[8:11], v2, s[6:7] offset:32
	global_load_dwordx4 v[12:15], v2, s[6:7] offset:64
	global_load_dwordx4 v[122:125], v2, s[6:7] offset:96
	v_add_f32_e32 v2, v227, v188
	v_add_f32_e32 v2, v186, v2
	v_add_f32_e32 v2, v189, v2
	v_add_f32_e32 v2, v185, v2
	v_add_f32_e32 v2, v187, v2
	v_add_f32_e32 v2, v183, v2
	v_add_f32_e32 v2, v184, v2
	v_add_f32_e32 v2, v179, v2
	v_add_f32_e32 v2, v182, v2
	v_add_f32_e32 v2, v144, v2
	v_add_f32_e32 v2, v180, v2
	v_exp_f32_e32 v16, v140
	v_add_f32_e32 v2, v142, v2
	v_exp_f32_e32 v17, v141
	v_add_f32_e32 v2, v181, v2
	v_exp_f32_e32 v138, v138
	v_add_f32_e32 v2, v143, v2
	v_exp_f32_e32 v139, v139
	v_add_f32_e32 v2, v145, v2
	v_exp_f32_e32 v136, v136
	v_add_f32_e32 v2, v16, v2
	v_exp_f32_e32 v137, v137
	v_add_f32_e32 v2, v17, v2
	v_exp_f32_e32 v140, v134
	v_add_f32_e32 v2, v138, v2
	v_exp_f32_e32 v141, v135
	v_add_f32_e32 v2, v139, v2
	v_exp_f32_e32 v190, v132
	v_add_f32_e32 v2, v136, v2
	v_exp_f32_e32 v192, v133
	v_add_f32_e32 v2, v137, v2
	v_exp_f32_e32 v193, v130
	v_add_f32_e32 v2, v140, v2
	v_exp_f32_e32 v194, v131
	v_add_f32_e32 v2, v141, v2
	v_exp_f32_e32 v195, v126
	v_add_f32_e32 v2, v190, v2
	v_exp_f32_e32 v196, v127
	v_add_f32_e32 v2, v192, v2
	v_exp_f32_e32 v197, v128
	v_add_f32_e32 v2, v193, v2
	v_exp_f32_e32 v198, v129
	v_add_f32_e32 v2, v194, v2
	v_add_f32_e32 v2, v195, v2
	v_add_f32_e32 v2, v196, v2
	v_add_f32_e32 v2, v197, v2
	v_add_f32_e32 v2, v198, v2
	v_mov_b32_e32 v126, v2
	s_nop 1
	v_permlane32_swap_b32_e32 v2, v126
	v_add_f32_e32 v2, v2, v126
	v_fmac_f32_e32 v2, v191, v220
	v_cvt_pk_bf16_f32 v126, v188, v227
	v_cvt_pk_bf16_f32 v127, v186, v189
	v_cvt_pk_bf16_f32 v128, v185, v187
	v_cvt_pk_bf16_f32 v129, v183, v184
	v_cvt_pk_bf16_f32 v130, v179, v182
	v_cvt_pk_bf16_f32 v131, v144, v180
	v_cvt_pk_bf16_f32 v132, v142, v181
	v_cvt_pk_bf16_f32 v133, v143, v145
	v_cvt_pk_bf16_f32 v134, v16, v17
	v_cvt_pk_bf16_f32 v135, v138, v139
	v_cvt_pk_bf16_f32 v136, v136, v137
	v_cvt_pk_bf16_f32 v137, v140, v141
	v_cvt_pk_bf16_f32 v138, v190, v192
	v_cvt_pk_bf16_f32 v139, v193, v194
	v_cvt_pk_bf16_f32 v140, v195, v196
	v_cvt_pk_bf16_f32 v141, v197, v198
	s_nop 0
	v_permlane32_swap_b32_e32 v126, v128
	v_permlane32_swap_b32_e32 v127, v129
	v_permlane32_swap_b32_e32 v130, v132
	v_permlane32_swap_b32_e32 v131, v133
	v_permlane32_swap_b32_e32 v134, v136
	v_permlane32_swap_b32_e32 v135, v137
	v_permlane32_swap_b32_e32 v138, v140
	v_permlane32_swap_b32_e32 v139, v141
	ds_read_b64_tr_b16 v[142:143], v209 offset:0
	ds_read_b64_tr_b16 v[144:145], v209 offset:0x800
	ds_read_b64_tr_b16 v[180:181], v209 offset:0x1000
	ds_read_b64_tr_b16 v[182:183], v209 offset:0x1800
	ds_read_b64_tr_b16 v[184:185], v209 offset:0x2000
	ds_read_b64_tr_b16 v[186:187], v209 offset:0x2800
	ds_read_b64_tr_b16 v[188:189], v209 offset:0x3000
	ds_read_b64_tr_b16 v[190:191], v209 offset:0x3800
	s_waitcnt lgkmcnt(0)
	s_nop 0
	v_mfma_f32_32x32x16_bf16 v[66:81], v[126:129], v[142:145], v[66:81]
	ds_read_b64_tr_b16 v[142:143], v209 offset:0x200
	ds_read_b64_tr_b16 v[144:145], v209 offset:0xa00
	v_mfma_f32_32x32x16_bf16 v[66:81], v[130:133], v[180:183], v[66:81]
	ds_read_b64_tr_b16 v[180:181], v209 offset:0x1200
	ds_read_b64_tr_b16 v[182:183], v209 offset:0x1a00
	v_mfma_f32_32x32x16_bf16 v[66:81], v[134:137], v[184:187], v[66:81]
	ds_read_b64_tr_b16 v[184:185], v209 offset:0x2200
	ds_read_b64_tr_b16 v[186:187], v209 offset:0x2a00
	ds_read_b64_tr_b16 v[192:193], v209 offset:0x3200
	ds_read_b64_tr_b16 v[194:195], v209 offset:0x3a00
	s_waitcnt lgkmcnt(0)
	v_mfma_f32_32x32x16_bf16 v[66:81], v[138:141], v[188:191], v[66:81]
	v_mfma_f32_32x32x16_bf16 v[50:65], v[126:129], v[142:145], v[50:65]
	ds_read_b64_tr_b16 v[142:143], v209 offset:0x400
	ds_read_b64_tr_b16 v[144:145], v209 offset:0xc00
	v_mfma_f32_32x32x16_bf16 v[50:65], v[130:133], v[180:183], v[50:65]
	ds_read_b64_tr_b16 v[180:181], v209 offset:0x1400
	ds_read_b64_tr_b16 v[182:183], v209 offset:0x1c00
	v_mfma_f32_32x32x16_bf16 v[50:65], v[134:137], v[184:187], v[50:65]
	ds_read_b64_tr_b16 v[184:185], v209 offset:0x2400
	ds_read_b64_tr_b16 v[186:187], v209 offset:0x2c00
	ds_read_b64_tr_b16 v[188:189], v209 offset:0x3400
	ds_read_b64_tr_b16 v[190:191], v209 offset:0x3c00
	s_waitcnt lgkmcnt(0)
	v_mfma_f32_32x32x16_bf16 v[50:65], v[138:141], v[192:195], v[50:65]
	v_mfma_f32_32x32x16_bf16 v[34:49], v[126:129], v[142:145], v[34:49]
	ds_read_b64_tr_b16 v[142:143], v209 offset:0x600
	ds_read_b64_tr_b16 v[144:145], v209 offset:0xe00
	v_mfma_f32_32x32x16_bf16 v[34:49], v[130:133], v[180:183], v[34:49]
	ds_read_b64_tr_b16 v[180:181], v209 offset:0x1600
	ds_read_b64_tr_b16 v[182:183], v209 offset:0x1e00
	v_mfma_f32_32x32x16_bf16 v[34:49], v[134:137], v[184:187], v[34:49]
	ds_read_b64_tr_b16 v[184:185], v209 offset:0x2600
	ds_read_b64_tr_b16 v[186:187], v209 offset:0x2e00
	ds_read_b64_tr_b16 v[192:193], v209 offset:0x3600
	ds_read_b64_tr_b16 v[194:195], v209 offset:0x3e00
	s_waitcnt lgkmcnt(0)
	v_mfma_f32_32x32x16_bf16 v[34:49], v[138:141], v[188:191], v[34:49]
	v_mfma_f32_32x32x16_bf16 v[18:33], v[126:129], v[142:145], v[18:33]
	s_andn2_b64 vcc, exec, s[4:5]
	v_mfma_f32_32x32x16_bf16 v[18:33], v[130:133], v[180:183], v[18:33]
	v_mfma_f32_32x32x16_bf16 v[18:33], v[134:137], v[184:187], v[18:33]
	v_mfma_f32_32x32x16_bf16 v[18:33], v[138:141], v[192:195], v[18:33]
	s_cbranch_vccnz .LBB0_1062
; __device__ __forceinline__ void mask_tile(f32x16& p0, f32x16& p1, int dq, unsigned W) {
;     const float NEG = -__builtin_inff();
; #pragma unroll
;     for (int r = 0; r < 16; ++r) {
;         const int c = (r & 3) + 8 * (r >> 2);
;         if ((unsigned)(dq - c) >= W) p0[r] = NEG;
;         if ((unsigned)(dq - c - 32) >= W) p1[r] = NEG;
;     }
; }
	s_lshl_b32 s5, s41, 6
	s_sub_i32 s4, s5, 64
	s_add_i32 s5, s5, -1
	s_cmp_le_i32 s5, s40
	s_cselect_b64 s[6:7], -1, 0
	s_cmp_gt_i32 s4, s60
	s_cselect_b64 s[36:37], -1, 0
	s_and_b64 s[6:7], s[6:7], s[36:37]
	s_and_b64 vcc, exec, s[6:7]
	s_cbranch_vccnz .LBB0_1057
	v_subrev_u32_e32 v16, s4, v210
	v_cmp_gt_u32_e32 vcc, 2.0, v16
	v_subrev_u32_e32 v17, 32, v16
	s_nop 0
	v_cndmask_b32_e32 v82, v200, v82, vcc
	v_cmp_gt_u32_e32 vcc, 2.0, v17
	v_add_u32_e32 v17, -1, v16
	s_nop 0
	v_cndmask_b32_e32 v98, v200, v98, vcc
	v_cmp_gt_u32_e32 vcc, 2.0, v17
	v_subrev_u32_e32 v17, 33, v16
	s_nop 0
	v_cndmask_b32_e32 v83, v200, v83, vcc
	v_cmp_gt_u32_e32 vcc, 2.0, v17
	v_add_u32_e32 v17, -2, v16
	s_nop 0
	v_cndmask_b32_e32 v99, v200, v99, vcc
	v_cmp_gt_u32_e32 vcc, 2.0, v17
	v_subrev_u32_e32 v17, 34, v16
	s_nop 0
	v_cndmask_b32_e32 v84, v200, v84, vcc
	v_cmp_gt_u32_e32 vcc, 2.0, v17
	v_add_u32_e32 v17, -3, v16
	s_nop 0
	v_cndmask_b32_e32 v100, v200, v100, vcc
	v_cmp_gt_u32_e32 vcc, 2.0, v17
	v_subrev_u32_e32 v17, 35, v16
	s_nop 0
	v_cndmask_b32_e32 v85, v200, v85, vcc
	v_cmp_gt_u32_e32 vcc, 2.0, v17
	v_add_u32_e32 v17, -8, v16
	s_nop 0
	v_cndmask_b32_e32 v101, v200, v101, vcc
	v_cmp_gt_u32_e32 vcc, 2.0, v17
	v_subrev_u32_e32 v17, 40, v16
	s_nop 0
	v_cndmask_b32_e32 v86, v200, v86, vcc
	v_cmp_gt_u32_e32 vcc, 2.0, v17
	v_add_u32_e32 v17, -9, v16
	s_nop 0
	v_cndmask_b32_e32 v102, v200, v102, vcc
	v_cmp_gt_u32_e32 vcc, 2.0, v17
	v_subrev_u32_e32 v17, 41, v16
	s_nop 0
	v_cndmask_b32_e32 v87, v200, v87, vcc
	v_cmp_gt_u32_e32 vcc, 2.0, v17
	v_add_u32_e32 v17, -10, v16
	s_nop 0
	v_cndmask_b32_e32 v103, v200, v103, vcc
	v_cmp_gt_u32_e32 vcc, 2.0, v17
	v_subrev_u32_e32 v17, 42, v16
	s_nop 0
	v_cndmask_b32_e32 v88, v200, v88, vcc
	v_cmp_gt_u32_e32 vcc, 2.0, v17
	v_add_u32_e32 v17, -11, v16
	s_nop 0
	v_cndmask_b32_e32 v104, v200, v104, vcc
	v_cmp_gt_u32_e32 vcc, 2.0, v17
	v_subrev_u32_e32 v17, 43, v16
	s_nop 0
	v_cndmask_b32_e32 v89, v200, v89, vcc
	v_cmp_gt_u32_e32 vcc, 2.0, v17
	v_add_u32_e32 v17, -16, v16
	s_nop 0
	v_cndmask_b32_e32 v105, v200, v105, vcc
	v_cmp_gt_u32_e32 vcc, 2.0, v17
	v_subrev_u32_e32 v17, 48, v16
	s_nop 0
	v_cndmask_b32_e32 v90, v200, v90, vcc
	v_cmp_gt_u32_e32 vcc, 2.0, v17
	v_subrev_u32_e32 v17, 17, v16
	s_nop 0
	v_cndmask_b32_e32 v106, v200, v106, vcc
	v_cmp_gt_u32_e32 vcc, 2.0, v17
	v_subrev_u32_e32 v17, 49, v16
	s_nop 0
	v_cndmask_b32_e32 v91, v200, v91, vcc
	v_cmp_gt_u32_e32 vcc, 2.0, v17
	v_subrev_u32_e32 v17, 18, v16
	s_nop 0
	v_cndmask_b32_e32 v107, v200, v107, vcc
	v_cmp_gt_u32_e32 vcc, 2.0, v17
	v_subrev_u32_e32 v17, 50, v16
	s_nop 0
	v_cndmask_b32_e32 v92, v200, v92, vcc
	v_cmp_gt_u32_e32 vcc, 2.0, v17
	v_subrev_u32_e32 v17, 19, v16
	s_nop 0
	v_cndmask_b32_e32 v108, v200, v108, vcc
	v_cmp_gt_u32_e32 vcc, 2.0, v17
	v_subrev_u32_e32 v17, 51, v16
	s_nop 0
	v_cndmask_b32_e32 v93, v200, v93, vcc
	v_cmp_gt_u32_e32 vcc, 2.0, v17
	v_subrev_u32_e32 v17, 24, v16
	s_nop 0
	v_cndmask_b32_e32 v109, v200, v109, vcc
	v_cmp_gt_u32_e32 vcc, 2.0, v17
	v_subrev_u32_e32 v17, 56, v16
	s_nop 0
	v_cndmask_b32_e32 v94, v200, v94, vcc
	v_cmp_gt_u32_e32 vcc, 2.0, v17
	v_subrev_u32_e32 v17, 25, v16
	s_nop 0
	v_cndmask_b32_e32 v110, v200, v110, vcc
	v_cmp_gt_u32_e32 vcc, 2.0, v17
	v_subrev_u32_e32 v17, 57, v16
	s_nop 0
	v_cndmask_b32_e32 v95, v200, v95, vcc
	v_cmp_gt_u32_e32 vcc, 2.0, v17
	v_subrev_u32_e32 v17, 26, v16
	s_nop 0
	v_cndmask_b32_e32 v111, v200, v111, vcc
	v_cmp_gt_u32_e32 vcc, 2.0, v17
	v_subrev_u32_e32 v17, 58, v16
	s_nop 0
	v_cndmask_b32_e32 v96, v200, v96, vcc
	v_cmp_gt_u32_e32 vcc, 2.0, v17
	v_subrev_u32_e32 v17, 27, v16
	v_subrev_u32_e32 v16, 59, v16
	v_cndmask_b32_e32 v112, v200, v112, vcc
	v_cmp_gt_u32_e32 vcc, 2.0, v17
	s_nop 1
	v_cndmask_b32_e32 v97, v200, v97, vcc
	v_cmp_gt_u32_e32 vcc, 2.0, v16
	s_nop 1
	v_cndmask_b32_e32 v113, v200, v113, vcc
